# mixer weight-conversion slots: waves 4-7 delayed once (s_sleep) at slot entry so SIMD partner waves alternate load-wait and convert instead of running in lockstep
# speedup vs baseline: 1.0209x; 1.0058x over previous
;     constexpr int N = (GRP == 0) ? CONV_N0 : (GRP == 1) ? CONV_N1 : (GRP == 2) ? CONV_N2 : (GRP == 3) ? CONV_N3 : CONV_N4;
;     for (int it = first + F.gw; it < N; it += F.NGW) conv_item<GRP>(F, it);
; }
; template <int L>
; __device__ __forceinline__ void layer(Frame& F, const XcdBarrier& bar, float* out, const int lo, const int hi) {
;     ...
;         if (cls == 0) { conv_all<GRP>(F, (F.G == 256) ? ((L == 0) ? SLOT_FIRST0 : SLOT_FIRST1) : 0); if (L == 0 && F.G == 256) { const int e4 = F.gw - G4_SLACK0; if (e4 >= 0 && e4 < G4_TAIL) conv_item<4>(F, 2048 + e4); } __syncthreads(); }
.LBB0_503:
	s_or_b64 exec, exec, s[0:1]
	v_readlane_b32 s0, v255, 27
	s_cmp_lg_u32 s0, 0
	s_waitcnt lgkmcnt(0)
	s_barrier
	s_cbranch_scc1 .LBB0_527
	s_cmpk_eq_i32 s48, 0x100
	s_cselect_b64 s[0:1], -1, 0
	s_and_b64 s[6:7], s[0:1], exec
	s_cselect_b32 s3, 0x15b0, 0
	v_readlane_b32 s4, v255, 10
	s_add_i32 s3, s3, s4
	s_cmpk_gt_i32 s3, 0x3c2f
	s_cbranch_scc1 .LBB0_524
	v_readlane_b32 s4, v255, 9
	s_mulk_i32 s4, 0x2200
	v_lshrrev_b32_e32 v1, 1, v0
	v_mov_b32_e32 v11, 0
	v_lshlrev_b32_e32 v10, 4, v194
	s_add_i32 s4, s4, 0
	v_and_b32_e32 v15, 28, v1
	v_lshl_add_u64 v[6:7], s[50:51], 0, v[10:11]
	s_mov_b64 s[10:11], 0xbbc00
	v_and_b32_e32 v1, 7, v0
	v_lshl_add_u64 v[12:13], v[6:7], 0, s[10:11]
	s_add_u32 s10, s50, 0x8b000
	v_lshlrev_b32_e32 v14, 2, v1
	v_mul_u32_u24_e32 v23, 0x210, v1
	v_lshlrev_b32_e32 v16, 4, v1
	v_mbcnt_lo_u32_b32 v1, -1, 0
	v_lshlrev_b32_e32 v2, 2, v194
	s_addc_u32 s11, s51, 0
	v_lshrrev_b32_e32 v20, 3, v194
	v_mov_b32_e32 v17, v11
	v_mbcnt_hi_u32_b32 v30, -1, v1
	v_and_b32_e32 v4, 28, v2
	s_add_u32 s12, s50, 0x13200000
	v_lshlrev_b32_e32 v21, 2, v20
	v_lshl_add_u64 v[6:7], s[50:51], 0, v[16:17]
	s_mov_b64 s[14:15], 0x3400000
	v_readlane_b32 s8, v255, 13
	v_and_b32_e32 v1, 64, v30
	s_mov_b32 s9, 0
	v_cmp_gt_u32_e64 s[6:7], 8, v194
	s_addc_u32 s13, s51, 0
	v_add_u32_e32 v22, s4, v21
	v_add_u32_e32 v24, s4, v16
	v_mul_u32_u24_e32 v25, 0x84, v20
	v_or_b32_e32 v26, 8, v20
	v_or_b32_e32 v27, 16, v20
	v_or_b32_e32 v28, 24, v20
	v_lshl_add_u64 v[18:19], v[6:7], 0, s[14:15]
	s_lshl_b32 s4, s3, 5
	s_lshl_b32 s22, s8, 5
	s_add_i32 s23, 0, 0x20240
	s_movk_i32 s24, 0x4c20
	s_movk_i32 s25, 0xa0
	s_movk_i32 s26, 0x2000
	s_movk_i32 s27, 0x5000
	s_mov_b32 s28, 0x8000
	s_mov_b32 s29, 0x58000
	s_mov_b32 s30, 0x5a000
	s_mov_b32 s31, 0x5d000
	s_mov_b32 s34, 0x60000
	s_mov_b32 s35, 0xb0000
	s_mov_b32 s36, 0xb2000
	s_mov_b32 s37, 0xb5000
	s_mov_b32 s38, 0xb8000
	s_mov_b32 s39, 0x108000
	s_mov_b32 s40, 0x10a000
	s_mov_b32 s41, 0x10d000
	s_mov_b32 s42, 0x110000
	v_lshlrev_b32_e32 v29, 2, v2
	s_add_i32 s43, 0, 0x202b0
	s_movk_i32 s44, 0x4000
	s_movk_i32 s45, 0x6000
	s_mov_b32 s46, 0x40000
	s_mov_b32 s47, 0x42000
	s_mov_b32 s49, 0x44000
	s_mov_b32 s52, 0x46000
	s_mov_b32 s53, 0x80000
	s_mov_b32 s54, 0x82000
	s_mov_b32 s55, 0x84000
	s_mov_b32 s56, 0x86000
	s_mov_b32 s57, 0xc0000
	s_mov_b32 s62, 0xc2000
	s_mov_b32 s63, 0xc4000
	s_mov_b32 s66, 0xc6000
	s_mov_b32 s67, 0xc3e00000
	s_add_i32 s68, 0, 0x20248
	s_mov_b64 s[14:15], 0x1000000
	v_lshlrev_b32_e32 v10, 2, v4
	v_xor_b32_e32 v31, 8, v30
	v_add_u32_e32 v32, 64, v1
	v_xor_b32_e32 v33, 16, v30
	s_waitcnt vmcnt(14)
	v_xor_b32_e32 v34, 32, v30
	v_mov_b32_e32 v35, 0x580000
	v_mov_b32_e32 v36, 0x1600
	v_mov_b32_e32 v37, 0x43e00000
	v_readlane_b32 s16, v255, 9
	s_cmp_lt_u32 s16, 4
	s_cbranch_scc1 .Lstg_507
	s_sleep 44
.Lstg_507:
	s_branch .LBB0_507

; template <int L>
; __device__ __forceinline__ void layer(Frame& F, const XcdBarrier& bar, float* out, const int lo, const int hi) {
;     ...
;         if (cls == 1) { conv_all<GRP>(F, (F.G == 256) ? ((L == 0) ? SLOT_FIRST0 : SLOT_FIRST1) : 0); if (L == 0 && F.G == 256) { const int e4 = F.gw - G4_SLACK0; if (e4 >= 0 && e4 < G4_TAIL) conv_item<4>(F, 2048 + e4); } __syncthreads(); }
.LBB0_620:
	v_readlane_b32 s0, v255, 27
	s_cmp_lg_u32 s0, 1
	s_barrier
	s_cbranch_scc1 .LBB0_644
	s_cmpk_eq_i32 s48, 0x100
	s_cselect_b64 s[0:1], -1, 0
	s_and_b64 s[6:7], s[0:1], exec
	s_cselect_b32 s3, 0x15b0, 0
	v_readlane_b32 s4, v255, 10
	s_add_i32 s3, s3, s4
	s_cmpk_gt_i32 s3, 0x3c2f
	s_mov_b32 s9, 0
	s_cbranch_scc1 .LBB0_641
	v_readlane_b32 s4, v255, 9
	s_mulk_i32 s4, 0x2200
	v_lshrrev_b32_e32 v1, 1, v0
	v_mov_b32_e32 v11, 0
	v_lshlrev_b32_e32 v10, 4, v194
	s_add_i32 s4, s4, 0
	v_and_b32_e32 v15, 28, v1
	v_lshl_add_u64 v[6:7], s[50:51], 0, v[10:11]
	s_mov_b64 s[10:11], 0xbbc00
	v_and_b32_e32 v1, 7, v0
	v_lshl_add_u64 v[12:13], v[6:7], 0, s[10:11]
	s_add_u32 s10, s50, 0x8b000
	v_lshlrev_b32_e32 v14, 2, v1
	v_mul_u32_u24_e32 v23, 0x210, v1
	v_lshlrev_b32_e32 v16, 4, v1
	v_mbcnt_lo_u32_b32 v1, -1, 0
	v_lshlrev_b32_e32 v2, 2, v194
	s_addc_u32 s11, s51, 0
	v_lshrrev_b32_e32 v20, 3, v194
	v_mov_b32_e32 v17, v11
	v_mbcnt_hi_u32_b32 v30, -1, v1
	v_and_b32_e32 v4, 28, v2
	s_add_u32 s12, s50, 0x13200000
	v_lshlrev_b32_e32 v21, 2, v20
	v_lshl_add_u64 v[6:7], s[50:51], 0, v[16:17]
	s_mov_b64 s[14:15], 0x3400000
	v_readlane_b32 s8, v255, 13
	v_and_b32_e32 v1, 64, v30
	v_cmp_gt_u32_e64 s[6:7], 8, v194
	s_addc_u32 s13, s51, 0
	v_add_u32_e32 v22, s4, v21
	v_add_u32_e32 v24, s4, v16
	v_mul_u32_u24_e32 v25, 0x84, v20
	v_or_b32_e32 v26, 8, v20
	v_or_b32_e32 v27, 16, v20
	v_or_b32_e32 v28, 24, v20
	v_lshl_add_u64 v[18:19], v[6:7], 0, s[14:15]
	s_lshl_b32 s4, s3, 5
	s_lshl_b32 s22, s8, 5
	s_add_i32 s23, 0, 0x20240
	s_movk_i32 s24, 0x4c20
	s_movk_i32 s25, 0x2000
	s_mov_b32 s26, 0x8000
	s_mov_b32 s27, 0x58000
	s_mov_b32 s28, 0x5a000
	s_mov_b32 s29, 0x5d000
	s_mov_b32 s30, 0x60000
	s_mov_b32 s31, 0xb0000
	s_mov_b32 s34, 0xb2000
	s_mov_b32 s35, 0xb5000
	s_mov_b32 s36, 0xb8000
	s_mov_b32 s37, 0x108000
	s_mov_b32 s38, 0x10a000
	s_mov_b32 s39, 0x10d000
	s_mov_b32 s40, 0x110000
	v_lshlrev_b32_e32 v29, 2, v2
	s_add_i32 s41, 0, 0x202b0
	s_movk_i32 s42, 0x4000
	s_movk_i32 s43, 0x6000
	s_mov_b32 s44, 0x40000
	s_mov_b32 s45, 0x42000
	s_mov_b32 s46, 0x44000
	s_mov_b32 s47, 0x46000
	s_mov_b32 s49, 0x80000
	s_mov_b32 s52, 0x82000
	s_mov_b32 s53, 0x84000
	s_mov_b32 s54, 0x86000
	s_mov_b32 s55, 0xc0000
	s_mov_b32 s56, 0xc2000
	s_mov_b32 s57, 0xc4000
	s_mov_b32 s62, 0xc6000
	s_mov_b32 s63, 0xc3e00000
	s_add_i32 s66, 0, 0x20248
	s_mov_b64 s[14:15], 0x1000000
	v_lshlrev_b32_e32 v10, 2, v4
	v_xor_b32_e32 v31, 8, v30
	v_add_u32_e32 v32, 64, v1
	v_xor_b32_e32 v33, 16, v30
	s_waitcnt vmcnt(14)
	v_xor_b32_e32 v34, 32, v30
	v_mov_b32_e32 v35, 0x580000
	v_mov_b32_e32 v36, 0x1600
	v_mov_b32_e32 v37, 0x43e00000
	v_readlane_b32 s16, v255, 9
	s_cmp_lt_u32 s16, 4
	s_cbranch_scc1 .Lstg_624
	s_sleep 44

; template <int L>
; __device__ __forceinline__ void layer(Frame& F, const XcdBarrier& bar, float* out, const int lo, const int hi) {
;     ...
;         if (cls == 2) { conv_all<GRP>(F, (F.G == 256) ? ((L == 0) ? SLOT_FIRST0 : SLOT_FIRST1) : 0); if (L == 0 && F.G == 256) { const int e4 = F.gw - G4_SLACK0; if (e4 >= 0 && e4 < G4_TAIL) conv_item<4>(F, 2048 + e4); } __syncthreads(); }
.LBB0_778:
	v_readlane_b32 s0, v255, 27
	s_cmp_lg_u32 s0, 2
	s_barrier
	s_cbranch_scc1 .LBB0_802
	s_cmpk_eq_i32 s48, 0x100
	s_cselect_b64 s[0:1], -1, 0
	s_and_b64 s[6:7], s[0:1], exec
	s_cselect_b32 s3, 0x15b0, 0
	v_readlane_b32 s4, v255, 10
	s_add_i32 s3, s3, s4
	s_cmpk_gt_i32 s3, 0x3c2f
	s_mov_b32 s9, 0
	s_cbranch_scc1 .LBB0_799
	v_readlane_b32 s4, v255, 9
	s_mulk_i32 s4, 0x2200
	v_lshrrev_b32_e32 v1, 1, v0
	v_mov_b32_e32 v11, 0
	v_lshlrev_b32_e32 v10, 4, v194
	s_add_i32 s4, s4, 0
	v_and_b32_e32 v15, 28, v1
	v_lshl_add_u64 v[6:7], s[50:51], 0, v[10:11]
	s_mov_b64 s[10:11], 0xbbc00
	v_and_b32_e32 v1, 7, v0
	v_lshl_add_u64 v[12:13], v[6:7], 0, s[10:11]
	s_add_u32 s10, s50, 0x8b000
	v_lshlrev_b32_e32 v14, 2, v1
	v_mul_u32_u24_e32 v23, 0x210, v1
	v_lshlrev_b32_e32 v16, 4, v1
	v_mbcnt_lo_u32_b32 v1, -1, 0
	v_lshlrev_b32_e32 v2, 2, v194
	s_addc_u32 s11, s51, 0
	v_lshrrev_b32_e32 v20, 3, v194
	v_mov_b32_e32 v17, v11
	v_mbcnt_hi_u32_b32 v30, -1, v1
	v_and_b32_e32 v4, 28, v2
	s_add_u32 s12, s50, 0x13200000
	v_lshlrev_b32_e32 v21, 2, v20
	v_lshl_add_u64 v[6:7], s[50:51], 0, v[16:17]
	s_mov_b64 s[14:15], 0x3400000
	v_readlane_b32 s8, v255, 13
	v_and_b32_e32 v1, 64, v30
	v_cmp_gt_u32_e64 s[6:7], 8, v194
	s_addc_u32 s13, s51, 0
	v_add_u32_e32 v22, s4, v21
	v_add_u32_e32 v24, s4, v16
	v_mul_u32_u24_e32 v25, 0x84, v20
	v_or_b32_e32 v26, 8, v20
	v_or_b32_e32 v27, 16, v20
	v_or_b32_e32 v28, 24, v20
	v_lshl_add_u64 v[18:19], v[6:7], 0, s[14:15]
	s_lshl_b32 s4, s3, 5
	s_lshl_b32 s24, s8, 5
	s_add_i32 s25, 0, 0x20240
	s_movk_i32 s26, 0x4c20
	s_movk_i32 s27, 0x2000
	s_mov_b32 s28, 0x8000
	s_mov_b32 s29, 0x58000
	s_mov_b32 s30, 0x5a000
	s_mov_b32 s31, 0x5d000
	s_mov_b32 s34, 0x60000
	s_mov_b32 s35, 0xb0000
	s_mov_b32 s36, 0xb2000
	s_mov_b32 s37, 0xb5000
	s_mov_b32 s38, 0xb8000
	s_mov_b32 s39, 0x108000
	s_mov_b32 s40, 0x10a000
	s_mov_b32 s41, 0x10d000
	s_mov_b32 s42, 0x110000
	v_lshlrev_b32_e32 v29, 2, v2
	s_add_i32 s43, 0, 0x202b0
	s_movk_i32 s44, 0x4000
	s_movk_i32 s45, 0x6000
	s_mov_b32 s46, 0x40000
	s_mov_b32 s47, 0x42000
	s_mov_b32 s49, 0x44000
	s_mov_b32 s52, 0x46000
	s_mov_b32 s53, 0x80000
	s_mov_b32 s54, 0x82000
	s_mov_b32 s55, 0x84000
	s_mov_b32 s56, 0x86000
	s_mov_b32 s57, 0xc0000
	s_mov_b32 s62, 0xc2000
	s_mov_b32 s63, 0xc4000
	s_mov_b32 s66, 0xc6000
	s_mov_b32 s67, 0xc3e00000
	s_add_i32 s68, 0, 0x20248
	s_mov_b64 s[14:15], 0x1000000
	v_lshlrev_b32_e32 v10, 2, v4
	v_xor_b32_e32 v31, 8, v30
	v_add_u32_e32 v32, 64, v1
	v_xor_b32_e32 v33, 16, v30
	s_waitcnt vmcnt(15)
	v_xor_b32_e32 v34, 32, v30
	v_mov_b32_e32 v35, 0x580000
	v_mov_b32_e32 v36, 0x1600
	v_mov_b32_e32 v37, 0x43e00000
	v_readlane_b32 s16, v255, 9
	s_cmp_lt_u32 s16, 4
	s_cbranch_scc1 .Lstg_782
	s_sleep 44

; template <int GRP>
; __device__ __forceinline__ void conv_item(Frame& F, int r) {
;     unsigned char* scr = F.glds + F.wave * 8704; unsigned char* ws = F.ws;
;     float* cmx = (float*)(ws + WS_CTL + COLMAX_OFF);
;     if (GRP == 0 || GRP == 1 || GRP == 2 || GRP == 4) {
;         constexpr int l = (GRP == 2 || GRP == 4) ? 1 : 0;
;         constexpr bool QUANT = (GRP == 1 || GRP == 4); constexpr int NI = QUANT ? CI_WI : CS_WI;
;         if (r < NI) { const int kb = r / 152, nb = r % 152, c0 = (nb < 112) ? nb * 32 : SRC_GATE + 8 + (nb - 112) * 32, drow = nb * 32;
;             if (QUANT) cvt_item_i8(inptr(F, IN_WIN) + (size_t)l * D * NIN_SRC, NIN_SRC, kb * 128, c0, ws + WS_WIN + (size_t)l * NIN * D, D, drow, cmx + CMX_WIN + l * NIN + drow, scr, F.lane);
;             else colmax_item(inptr(F, IN_WIN) + (size_t)l * D * NIN_SRC, NIN_SRC, kb * 128, c0, cmx + CMX_WIN + l * NIN + drow, F.lane);
;             return; }
;         r -= NI;
;     }
;     if (GRP == 0 || GRP == 2) {
;         constexpr int l = (GRP == 2) ? 1 : 0;
;         if (r < CI_WO) { const int kb = r / 64, nb = r % 64;
;             cvt_item8(inptr(F, IN_WOUT) + (size_t)l * D * D, D, kb * 128, nb * 32, ws + WS_WOUT + (size_t)l * D * D, D, nb * 32, scr, F.lane); return; }
;         r -= CI_WO;
;         if (GRP == 0) {
;             if (r < CI_FD) { const int kb = r / 64, nb = r % 64; cvt_item8(inptr(F, IN_FD), D, kb * 128, nb * 32, ws + WS_WD, DFF, nb * 32, scr, F.lane); return; }
;             r -= CI_FD;
;         } else {
;             if (r < CI_MD) { const int e = r / (22 * 64); r %= (22 * 64); const int kb = r / 64, nb = r % 64;
;                 cvt_item8(inptr(F, IN_MD) + (size_t)e * DFE * D, D, kb * 128, nb * 32, ws + WS_MD + (size_t)e * D * DFE, DFE, nb * 32, scr, F.lane); return; }
;             r -= CI_MD;
;         }
;     }
;     if (GRP == 0 || GRP == 1) { constexpr int KBN = (GRP == 1) ? 16 : CMS_KB, I_F = KBN * 176; const int up = r / I_F; r %= I_F; const int kb = r / 176, nb = r % 176, n0 = nb * 32, drow = (n0 >> 7) * 256 + up * 128 + (n0 & 127);
;         if (GRP == 1) cvt_item_i8(inptr(F, up ? IN_FU : IN_FG), DFF, kb * 128, n0, ws + WS_WGU, D, drow, cmx + drow, scr, F.lane);
;         else colmax_item(inptr(F, up ? IN_FU : IN_FG), DFF, kb * 128, n0, cmx + drow, F.lane); }
.LBB0_922:
	v_readlane_b32 s0, v255, 27
	s_cmp_eq_u32 s0, 3
	s_barrier
	s_cbranch_scc0 .LBB0_946
	s_cmpk_eq_i32 s48, 0x100
	s_cselect_b64 s[0:1], -1, 0
	s_and_b64 s[6:7], s[0:1], exec
	s_cselect_b32 s3, 0x15b0, 0
	v_readlane_b32 s4, v255, 10
	s_add_i32 s3, s3, s4
	s_cmpk_gt_i32 s3, 0x3c2f
	s_mov_b32 s9, 0
	s_cbranch_scc1 .LBB0_943
	v_readlane_b32 s4, v255, 9
	s_mulk_i32 s4, 0x2200
	v_lshrrev_b32_e32 v1, 1, v0
	v_mov_b32_e32 v11, 0
	v_lshlrev_b32_e32 v10, 4, v194
	s_add_i32 s4, s4, 0
	v_and_b32_e32 v15, 28, v1
	v_lshl_add_u64 v[6:7], s[50:51], 0, v[10:11]
	s_mov_b64 s[10:11], 0xbbc00
	v_and_b32_e32 v1, 7, v0
	v_lshl_add_u64 v[12:13], v[6:7], 0, s[10:11]
	s_add_u32 s10, s50, 0x8b000
	v_lshlrev_b32_e32 v14, 2, v1
	v_mul_u32_u24_e32 v23, 0x210, v1
	v_lshlrev_b32_e32 v16, 4, v1
	v_mbcnt_lo_u32_b32 v1, -1, 0
	v_lshlrev_b32_e32 v2, 2, v194
	s_addc_u32 s11, s51, 0
	v_lshrrev_b32_e32 v20, 3, v194
	v_mov_b32_e32 v17, v11
	v_mbcnt_hi_u32_b32 v30, -1, v1
	v_and_b32_e32 v4, 28, v2
	s_add_u32 s12, s50, 0x13200000
	v_lshlrev_b32_e32 v21, 2, v20
	v_lshl_add_u64 v[6:7], s[50:51], 0, v[16:17]
	s_mov_b64 s[14:15], 0x3400000
	v_readlane_b32 s8, v255, 13
	v_and_b32_e32 v1, 64, v30
	v_cmp_gt_u32_e64 s[6:7], 8, v194
	s_addc_u32 s13, s51, 0
	v_add_u32_e32 v22, s4, v21
	v_add_u32_e32 v24, s4, v16
	v_mul_u32_u24_e32 v25, 0x84, v20
	v_or_b32_e32 v26, 8, v20
	v_or_b32_e32 v27, 16, v20
	v_or_b32_e32 v28, 24, v20
	v_lshl_add_u64 v[18:19], v[6:7], 0, s[14:15]
	s_lshl_b32 s4, s3, 5
	s_lshl_b32 s22, s8, 5
	s_add_i32 s23, 0, 0x20240
	s_movk_i32 s24, 0x4c20
	s_movk_i32 s25, 0xa0
	s_movk_i32 s26, 0x2000
	s_movk_i32 s27, 0x5000
	s_mov_b32 s28, 0x8000
	s_mov_b32 s29, 0x58000
	s_mov_b32 s30, 0x5a000
	s_mov_b32 s31, 0x5d000
	s_mov_b32 s34, 0x60000
	s_mov_b32 s35, 0xb0000
	s_mov_b32 s36, 0xb2000
	s_mov_b32 s37, 0xb5000
	s_mov_b32 s38, 0xb8000
	s_mov_b32 s39, 0x108000
	s_mov_b32 s40, 0x10a000
	s_mov_b32 s41, 0x10d000
	s_mov_b32 s42, 0x110000
	v_lshlrev_b32_e32 v29, 2, v2
	s_add_i32 s43, 0, 0x202b0
	s_movk_i32 s44, 0x4000
	s_movk_i32 s45, 0x6000
	s_mov_b32 s46, 0x40000
	s_mov_b32 s47, 0x42000
	s_mov_b32 s49, 0x44000
	s_mov_b32 s52, 0x46000
	s_mov_b32 s53, 0x80000
	s_mov_b32 s54, 0x82000
	s_mov_b32 s55, 0x84000
	s_mov_b32 s56, 0x86000
	s_mov_b32 s57, 0xc0000
	s_mov_b32 s62, 0xc2000
	s_mov_b32 s63, 0xc4000
	s_mov_b32 s66, 0xc6000
	s_mov_b32 s67, 0xc3e00000
	s_add_i32 s68, 0, 0x20248
	s_mov_b64 s[14:15], 0x1000000
	v_lshlrev_b32_e32 v10, 2, v4
	v_xor_b32_e32 v31, 8, v30
	v_add_u32_e32 v32, 64, v1
	v_xor_b32_e32 v33, 16, v30
	s_waitcnt vmcnt(15)
	v_xor_b32_e32 v34, 32, v30
	v_mov_b32_e32 v35, 0x580000
	v_mov_b32_e32 v36, 0x1600
	v_mov_b32_e32 v37, 0x43e00000
	v_readlane_b32 s16, v255, 9
	s_cmp_lt_u32 s16, 4
	s_cbranch_scc1 .Lstg_926
	s_sleep 44

; __device__ __forceinline__ void cvt_item_i8(const float* src, int ld, int k0, int c0, unsigned char* dst, int Kd, int drow0, const float* cmx  , unsigned char* scr, int lane) {
;     const int c = lane & 7, q = lane >> 3;
;     const f32x4 cm = *(const f32x4*)(cmx + 4 * c);
;     f32x4 inv; inv[0] = cm[0] > 0.f ? 127.f / cm[0] : 0.f; inv[1] = cm[1] > 0.f ? 127.f / cm[1] : 0.f; inv[2] = cm[2] > 0.f ? 127.f / cm[2] : 0.f; inv[3] = cm[3] > 0.f ? 127.f / cm[3] : 0.f;
;     f32x4 v[4][4];
; #pragma unroll
;     for (int g = 0; g < 4; ++g)
; #pragma unroll
;         for (int j = 0; j < 4; ++j) v[g][j] = __builtin_nontemporal_load((const f32x4*)(src + (size_t)(k0 + 32 * g + 4 * q + j) * ld + c0 + 4 * c));
; template <int GRP>
; __device__ __forceinline__ void conv_item(Frame& F, int r) {
;     ...
;     else { constexpr int KBN = (GRP == 3) ? 16 : CMS_KB, I_E = KBN * 88; const int up = r / (8 * I_E); r %= (8 * I_E); const int e = r / I_E; r %= I_E; const int kb = r / 88, nb = r % 88, n0 = nb * 32, drow = (n0 >> 7) * 256 + up * 128 + (n0 & 127);
;         if (GRP == 3) cvt_item_i8(inptr(F, up ? IN_MU : IN_MG) + (size_t)e * D * DFE, DFE, kb * 128, n0, ws + WS_MGU + (size_t)e * 2 * DFE * D, D, drow, cmx + 2 * DFF + e * 2 * DFE + drow, scr, F.lane);
;         else colmax_item(inptr(F, up ? IN_MU : IN_MG) + (size_t)e * D * DFE, DFE, kb * 128, n0, cmx + 2 * DFF + e * 2 * DFE + drow, F.lane); }
.LBB0_1669:
	s_or_b64 exec, exec, s[0:1]
	v_readlane_b32 s0, v255, 27
	s_cmp_lg_u32 s0, 0
	s_waitcnt lgkmcnt(0)
	s_barrier
	s_cbranch_scc1 .LBB0_1674
	s_cmpk_eq_i32 s48, 0x100
	s_cselect_b32 s0, 0x1800, 0
	v_readlane_b32 s1, v255, 10
	s_add_i32 s3, s0, s1
	s_cmpk_gt_i32 s3, 0x57ff
	v_readlane_b32 s40, v255, 13
	s_cbranch_scc1 .LBB0_1673
	v_readlane_b32 s0, v255, 9
	s_mulk_i32 s0, 0x2200
	s_add_i32 s0, s0, 0
	v_and_b32_e32 v2, 7, v0
	s_add_u32 s4, s50, 0x8200000
	v_lshrrev_b32_e32 v1, 3, v194
	v_lshlrev_b32_e32 v4, 2, v2
	v_mul_u32_u24_e32 v7, 0x210, v2
	v_lshlrev_b32_e32 v2, 4, v2
	s_addc_u32 s12, s51, 0
	v_lshlrev_b32_e32 v16, 2, v1
	v_add_u32_e32 v8, s0, v2
	v_mul_u32_u24_e32 v9, 0x84, v1
	s_add_u32 s13, s50, 0x8b000
	v_mov_b32_e32 v3, 0
	v_add_u32_e32 v6, s0, v16
	v_add_u32_e32 v22, v8, v9
	s_addc_u32 s14, s51, 0
	v_or_b32_e32 v17, 8, v1
	v_or_b32_e32 v18, 16, v1
	v_or_b32_e32 v19, 24, v1
	s_movk_i32 s15, 0xa0
	v_lshlrev_b32_e32 v4, 2, v4
	v_mov_b32_e32 v5, v3
	s_mov_b32 s16, 0x42fe0000
	s_movk_i32 s17, 0x2000
	s_movk_i32 s18, 0x5000
	s_mov_b32 s19, 0x8000
	s_mov_b32 s20, 0x58000
	s_mov_b32 s21, 0x5a000
	s_mov_b32 s22, 0x5d000
	s_mov_b32 s23, 0x60000
	s_mov_b32 s24, 0xb0000
	s_mov_b32 s25, 0xb2000
	s_mov_b32 s26, 0xb5000
	s_mov_b32 s27, 0xb8000
	s_mov_b32 s28, 0x108000
	s_mov_b32 s29, 0x10a000
	s_mov_b32 s30, 0x10d000
	s_mov_b32 s31, 0x110000
	s_mov_b32 s34, 0xc2fe0000
	v_mov_b32_e32 v20, 0x42fe0000
	s_mov_b32 s35, 0xc0c0500
	v_add_u32_e32 v21, v6, v7
	v_add_u32_e32 v23, 0x420, v22
	v_add_u32_e32 v24, 0x428, v22
	v_add_u32_e32 v25, 0x840, v22
	v_add_u32_e32 v26, 0x848, v22
	v_add_u32_e32 v27, 0xc60, v22
	v_add_u32_e32 v28, 0xc68, v22
	v_readlane_b32 s0, v255, 9
	s_cmp_lt_u32 s0, 4
	s_cbranch_scc1 .Lstg_1672
	s_sleep 44
.Lstg_1672:
.LBB0_1672:
	s_mul_hi_i32 s0, s3, 0x2e8ba2e9
	s_lshr_b32 s1, s0, 31
	s_ashr_i32 s0, s0, 11
	s_add_i32 s0, s0, s1
	s_mul_i32 s1, s0, 0xffffd400
	s_lshl_b32 s6, s0, 7
	s_add_i32 s0, s3, s1
	s_mul_i32 s1, s0, 0xba3
	s_lshr_b32 s7, s1, 31
	s_ashr_i32 s1, s1, 22
	s_add_i32 s1, s1, s7
	s_mul_i32 s7, s1, 0x580
	s_sub_i32 s0, s0, s7
	s_sext_i32_i16 s36, s0
	s_mulk_i32 s36, 0xba3
	s_lshr_b32 s38, s36, 31
	s_ashr_i32 s36, s36, 18
	s_add_i32 s38, s36, s38
	s_sext_i32_i16 s36, s38
	s_mulk_i32 s38, 0x58
	s_sub_i32 s0, s0, s38
	s_sext_i32_i16 s38, s0
	s_lshl_b32 s0, s38, 5
	s_lshl_b32 s38, s38, 6
	s_and_b32 s38, s38, 0xffffff00
	s_and_b32 s39, s0, 0x60
	s_add_i32 s38, s38, s6
	s_add_i32 s37, s3, 0x2bff
	s_or_b32 s6, s38, s39
	s_cmpk_lt_u32 s37, 0x57ff
	s_cselect_b32 s37, s15, 0xa8
	v_or_b32_e32 v8, s6, v17
	s_add_i32 s37, s37, 0
	v_ashrrev_i32_e32 v9, 31, v8
	s_add_i32 s37, s37, 0x20200
	v_lshlrev_b64 v[98:99], 11, v[8:9]
	v_mov_b32_e32 v8, s37
	ds_read_b64 v[8:9], v8
	s_sext_i32_i16 s11, s1
	s_mul_i32 s9, s11, 0x1600000
	s_mul_hi_i32 s1, s11, 0x1600000
	s_mul_i32 s10, s11, 0xb00000
	s_waitcnt lgkmcnt(0)
	v_readfirstlane_b32 s37, v8
	v_readfirstlane_b32 s38, v9
	s_add_u32 s9, s37, s9
	s_addc_u32 s37, s38, s1
	s_lshl_b32 s36, s36, 7
	s_mul_hi_i32 s7, s11, 0xb00000
	s_add_u32 s10, s4, s10
	s_mul_hi_i32 s8, s11, 0x5800
	s_mulk_i32 s11, 0x5800
	s_addc_u32 s38, s12, s7
	s_add_u32 s1, s13, s11
	s_addc_u32 s8, s14, s8
	s_ashr_i32 s7, s6, 31
	v_or_b32_e32 v6, s6, v1
	v_or_b32_e32 v10, s6, v18
	v_or_b32_e32 v12, s6, v19
	s_lshl_b64 s[6:7], s[6:7], 2
	s_add_u32 s6, s1, s6
	s_addc_u32 s7, s8, s7
	s_ashr_i32 s1, s0, 31
	s_lshl_b64 s[0:1], s[0:1], 2
	v_or_b32_e32 v8, s36, v16
	s_add_u32 s0, s9, s0
	v_ashrrev_i32_e32 v11, 31, v10
	v_mul_i32_i24_e32 v8, 0x2c00, v8
	s_addc_u32 s1, s37, s1
	v_lshlrev_b64 v[100:101], 11, v[10:11]
	v_ashrrev_i32_e32 v9, 31, v8
	v_lshl_add_u64 v[10:11], s[0:1], 0, v[4:5]
	v_ashrrev_i32_e32 v7, 31, v6
	v_ashrrev_i32_e32 v13, 31, v12
	v_lshl_add_u64 v[10:11], v[10:11], 0, v[8:9]
	v_lshlrev_b64 v[14:15], 11, v[6:7]
	v_lshlrev_b64 v[6:7], 11, v[12:13]
	v_add_co_u32_e32 v12, vcc, s17, v10
	global_load_dwordx4 v[30:33], v4, s[6:7]
	s_nop 0
	v_addc_co_u32_e32 v13, vcc, 0, v11, vcc
	v_add_co_u32_e32 v42, vcc, s18, v10
	s_ashr_i32 s6, s36, 31
	s_nop 0
	v_addc_co_u32_e32 v43, vcc, 0, v11, vcc
	v_add_co_u32_e32 v46, vcc, s19, v10
	s_add_u32 s0, s10, s36
	s_nop 0
	v_addc_co_u32_e32 v47, vcc, 0, v11, vcc
	v_add_co_u32_e32 v50, vcc, s20, v10
	s_addc_u32 s1, s38, s6
	s_nop 0
	v_addc_co_u32_e32 v51, vcc, 0, v11, vcc
	v_add_co_u32_e32 v54, vcc, s21, v10
	v_lshl_add_u64 v[8:9], s[0:1], 0, v[2:3]
	s_nop 0
	v_addc_co_u32_e32 v55, vcc, 0, v11, vcc
	v_add_co_u32_e32 v58, vcc, s22, v10
	v_lshl_add_u64 v[6:7], v[8:9], 0, v[6:7]
	s_nop 0
	v_addc_co_u32_e32 v59, vcc, 0, v11, vcc
	v_add_co_u32_e32 v62, vcc, s23, v10
	s_add_i32 s3, s3, s40
	s_nop 0
	v_addc_co_u32_e32 v63, vcc, 0, v11, vcc
	v_add_co_u32_e32 v66, vcc, s24, v10
	s_cmpk_lt_i32 s3, 0x5800
	s_nop 0
	v_addc_co_u32_e32 v67, vcc, 0, v11, vcc
	v_add_co_u32_e32 v70, vcc, s25, v10
	s_nop 0
	s_nop 0
	v_addc_co_u32_e32 v71, vcc, 0, v11, vcc
	v_add_co_u32_e32 v74, vcc, s26, v10
	s_nop 0
	s_nop 0
	v_addc_co_u32_e32 v75, vcc, 0, v11, vcc
	v_add_co_u32_e32 v78, vcc, s27, v10
	s_nop 0
	s_nop 0
	v_addc_co_u32_e32 v79, vcc, 0, v11, vcc
	v_add_co_u32_e32 v82, vcc, s28, v10
	s_nop 0
	s_nop 0
	v_addc_co_u32_e32 v83, vcc, 0, v11, vcc
	v_add_co_u32_e32 v86, vcc, s29, v10
	s_nop 0
	s_nop 0
	v_addc_co_u32_e32 v87, vcc, 0, v11, vcc
	v_add_co_u32_e32 v90, vcc, s30, v10
	s_nop 0
	s_nop 0
	v_addc_co_u32_e32 v91, vcc, 0, v11, vcc
	v_add_co_u32_e32 v94, vcc, s31, v10
	s_nop 0
	s_nop 0
	v_addc_co_u32_e32 v95, vcc, 0, v11, vcc
	global_load_dwordx4 v[34:37], v[10:11], off nt
	global_load_dwordx4 v[38:41], v[12:13], off offset:3072 nt
	s_nop 0
	global_load_dwordx4 v[42:45], v[42:43], off offset:2048 nt
	s_nop 0
	global_load_dwordx4 v[46:49], v[46:47], off offset:1024 nt
	s_nop 0
	global_load_dwordx4 v[50:53], v[50:51], off nt
	s_nop 0
	global_load_dwordx4 v[54:57], v[54:55], off offset:3072 nt
	s_nop 0
	global_load_dwordx4 v[58:61], v[58:59], off offset:2048 nt
	s_nop 0
	global_load_dwordx4 v[62:65], v[62:63], off offset:1024 nt
	s_nop 0
	global_load_dwordx4 v[66:69], v[66:67], off nt
	s_nop 0
	global_load_dwordx4 v[70:73], v[70:71], off offset:3072 nt
	s_nop 0
	global_load_dwordx4 v[74:77], v[74:75], off offset:2048 nt
	s_nop 0
	global_load_dwordx4 v[78:81], v[78:79], off offset:1024 nt
	s_nop 0
	global_load_dwordx4 v[82:85], v[82:83], off nt
	s_nop 0
	global_load_dwordx4 v[86:89], v[86:87], off offset:3072 nt
	s_nop 0
	global_load_dwordx4 v[90:93], v[90:91], off offset:2048 nt
	s_nop 0
	global_load_dwordx4 v[94:97], v[94:95], off offset:1024 nt
	s_waitcnt vmcnt(16)
; __device__ __forceinline__ unsigned pack_i8x4(float a, float b, float c, float d) {
;     const int ia = (int)rintf(fminf(fmaxf(a, -127.f), 127.f)), ib = (int)rintf(fminf(fmaxf(b, -127.f), 127.f)), ic = (int)rintf(fminf(fmaxf(c, -127.f), 127.f)), id = (int)rintf(fminf(fmaxf(d, -127.f), 127.f));
;     return (unsigned)(ia & 0xff) | ((unsigned)(ib & 0xff) << 8) | ((unsigned)(ic & 0xff) << 16) | ((unsigned)(id & 0xff) << 24);
; }
; __device__ __forceinline__ void cvt_item_i8(const float* src, int ld, int k0, int c0, unsigned char* dst, int Kd, int drow0, const float* cmx  , unsigned char* scr, int lane) {
;     const int c = lane & 7, q = lane >> 3;
;     const f32x4 cm = *(const f32x4*)(cmx + 4 * c);
;     f32x4 inv; inv[0] = cm[0] > 0.f ? 127.f / cm[0] : 0.f; inv[1] = cm[1] > 0.f ? 127.f / cm[1] : 0.f; inv[2] = cm[2] > 0.f ? 127.f / cm[2] : 0.f; inv[3] = cm[3] > 0.f ? 127.f / cm[3] : 0.f;
;     f32x4 v[4][4];
; #pragma unroll
;     for (int g = 0; g < 4; ++g)
; #pragma unroll
;         for (int j = 0; j < 4; ++j) v[g][j] = __builtin_nontemporal_load((const f32x4*)(src + (size_t)(k0 + 32 * g + 4 * q + j) * ld + c0 + 4 * c));
; #pragma unroll
;     for (int g = 0; g < 4; ++g)
; #pragma unroll
;         for (int i = 0; i < 4; ++i) *(unsigned*)(scr + (4 * c + i) * 132 + 32 * g + 4 * q) = pack_i8x4(v[g][0][i] * inv[i], v[g][1][i] * inv[i], v[g][2][i] * inv[i], v[g][3][i] * inv[i]);
	v_div_scale_f32 v29, s[0:1], v30, v30, s16
	v_rcp_f32_e32 v105, v29
	v_div_scale_f32 v103, s[0:1], v33, v33, s16
	v_fma_f32 v109, -v29, v105, 1.0
	v_rcp_f32_e32 v108, v103
	v_fmac_f32_e32 v105, v109, v105
	v_div_scale_f32 v102, s[8:9], s16, v32, s16
	v_lshl_add_u64 v[12:13], v[8:9], 0, v[98:99]
	v_div_scale_f32 v99, s[0:1], v31, v31, s16
	v_rcp_f32_e32 v106, v99
	v_lshl_add_u64 v[10:11], v[8:9], 0, v[14:15]
	v_lshl_add_u64 v[14:15], v[8:9], 0, v[100:101]
	v_div_scale_f32 v101, s[0:1], v32, v32, s16
	v_rcp_f32_e32 v107, v101
	v_div_scale_f32 v98, vcc, s16, v30, s16
	v_fma_f32 v110, -v99, v106, 1.0
	v_div_scale_f32 v100, s[6:7], s16, v31, s16
	v_fmac_f32_e32 v106, v110, v106
	v_mul_f32_e32 v109, v98, v105
	v_fma_f32 v111, -v101, v107, 1.0
	v_mul_f32_e32 v110, v100, v106
	v_fma_f32 v113, -v29, v109, v98
	v_fmac_f32_e32 v107, v111, v107
	v_fma_f32 v114, -v99, v110, v100
	v_fmac_f32_e32 v109, v113, v105
	v_fma_f32 v112, -v103, v108, 1.0
	v_mul_f32_e32 v111, v102, v107
	v_fmac_f32_e32 v110, v114, v106
	v_fma_f32 v29, -v29, v109, v98
	v_div_scale_f32 v104, s[10:11], s16, v33, s16
	v_fmac_f32_e32 v108, v112, v108
	v_fma_f32 v115, -v101, v111, v102
	v_fma_f32 v98, -v99, v110, v100
	v_div_fmas_f32 v29, v29, v105, v109
	s_mov_b64 vcc, s[6:7]
	v_mul_f32_e32 v112, v104, v108
	v_fmac_f32_e32 v111, v115, v107
	v_div_fixup_f32 v29, v29, v30, s16
	v_div_fmas_f32 v98, v98, v106, v110
	v_cmp_lt_f32_e32 vcc, 0, v30
	v_fma_f32 v116, -v103, v112, v104
	v_fma_f32 v99, -v101, v111, v102
	v_cndmask_b32_e32 v29, 0, v29, vcc
	s_mov_b64 vcc, s[8:9]
	v_fmac_f32_e32 v112, v116, v108
	v_div_fixup_f32 v30, v98, v31, s16
	v_div_fmas_f32 v98, v99, v107, v111
	v_cmp_lt_f32_e32 vcc, 0, v31
	v_fma_f32 v100, -v103, v112, v104
	v_div_fixup_f32 v31, v98, v32, s16
	v_cndmask_b32_e32 v30, 0, v30, vcc
	s_mov_b64 vcc, s[10:11]
	v_div_fmas_f32 v98, v100, v108, v112
	v_cmp_lt_f32_e32 vcc, 0, v32
	v_div_fixup_f32 v32, v98, v33, s16
	s_waitcnt vmcnt(0) lgkmcnt(0)
	v_mul_f32_e32 v34, v34, v29
	v_mul_f32_e32 v38, v29, v38
	v_mul_f32_e32 v42, v29, v42
	v_mul_f32_e32 v46, v29, v46
	v_mul_f32_e32 v50, v29, v50
	v_mul_f32_e32 v54, v29, v54
	v_mul_f32_e32 v58, v29, v58
	v_mul_f32_e32 v62, v29, v62
	v_mul_f32_e32 v66, v29, v66
	v_mul_f32_e32 v70, v29, v70
	v_mul_f32_e32 v74, v29, v74
	v_mul_f32_e32 v78, v29, v78
	v_mul_f32_e32 v82, v29, v82
	v_mul_f32_e32 v86, v29, v86
	v_cndmask_b32_e32 v31, 0, v31, vcc
	v_med3_f32 v34, v34, s34, v20
	v_med3_f32 v38, v38, s34, v20
	v_med3_f32 v42, v42, s34, v20
	v_med3_f32 v46, v46, s34, v20
	v_mul_f32_e32 v39, v30, v39
	v_mul_f32_e32 v43, v30, v43
	v_mul_f32_e32 v47, v30, v47
	v_med3_f32 v50, v50, s34, v20
	v_med3_f32 v54, v54, s34, v20
	v_mul_f32_e32 v55, v30, v55
	v_cmp_lt_f32_e32 vcc, 0, v33
	v_mul_f32_e32 v90, v29, v90
	v_mul_f32_e32 v35, v35, v30
	v_med3_f32 v58, v58, s34, v20
	v_med3_f32 v62, v62, s34, v20
	v_mul_f32_e32 v51, v30, v51
	v_mul_f32_e32 v59, v30, v59
	v_mul_f32_e32 v63, v30, v63
	v_med3_f32 v66, v66, s34, v20
	v_med3_f32 v70, v70, s34, v20
	v_med3_f32 v74, v74, s34, v20
	v_med3_f32 v78, v78, s34, v20
	v_mul_f32_e32 v71, v30, v71
	v_mul_f32_e32 v79, v30, v79
	v_med3_f32 v82, v82, s34, v20
	v_med3_f32 v86, v86, s34, v20
	v_mul_f32_e32 v87, v30, v87
	v_cndmask_b32_e32 v32, 0, v32, vcc
	v_rndne_f32_e32 v33, v34
	v_rndne_f32_e32 v34, v38
	v_rndne_f32_e32 v38, v42
	v_rndne_f32_e32 v42, v46
	v_med3_f32 v39, v39, s34, v20
	v_med3_f32 v43, v43, s34, v20
	v_med3_f32 v46, v47, s34, v20
	v_mul_f32_e32 v40, v31, v40
	v_mul_f32_e32 v47, v31, v48
	v_rndne_f32_e32 v48, v50
	v_rndne_f32_e32 v50, v54
	v_med3_f32 v55, v55, s34, v20
	v_mul_f32_e32 v56, v31, v56
	v_mul_f32_e32 v29, v29, v94
	v_mul_f32_e32 v67, v30, v67
	v_mul_f32_e32 v75, v30, v75
	v_med3_f32 v90, v90, s34, v20
	v_mul_f32_e32 v83, v30, v83
	v_mul_f32_e32 v91, v30, v91
	v_med3_f32 v35, v35, s34, v20
	v_mul_f32_e32 v36, v36, v31
	v_mul_f32_e32 v44, v31, v44
	v_rndne_f32_e32 v54, v58
	v_rndne_f32_e32 v58, v62
	v_med3_f32 v51, v51, s34, v20
	v_med3_f32 v59, v59, s34, v20
	v_med3_f32 v62, v63, s34, v20
	v_mul_f32_e32 v52, v31, v52
	v_mul_f32_e32 v60, v31, v60
	v_mul_f32_e32 v63, v31, v64
	v_rndne_f32_e32 v64, v66
	v_rndne_f32_e32 v66, v70
	v_rndne_f32_e32 v70, v74
	v_rndne_f32_e32 v74, v78
	v_med3_f32 v71, v71, s34, v20
	v_med3_f32 v78, v79, s34, v20
	v_mul_f32_e32 v72, v31, v72
	v_mul_f32_e32 v79, v31, v80
	v_rndne_f32_e32 v80, v82
	v_rndne_f32_e32 v82, v86
	v_med3_f32 v87, v87, s34, v20
	v_mul_f32_e32 v88, v31, v88
	v_cvt_i32_f32_e32 v34, v34
	v_rndne_f32_e32 v39, v39
	v_rndne_f32_e32 v43, v43
	v_med3_f32 v40, v40, s34, v20
	v_mul_f32_e32 v41, v32, v41
	v_cvt_i32_f32_e32 v50, v50
	v_rndne_f32_e32 v55, v55
	v_med3_f32 v56, v56, s34, v20
	v_mul_f32_e32 v57, v32, v57
	v_med3_f32 v29, v29, s34, v20
	v_mul_f32_e32 v30, v30, v95
	v_med3_f32 v67, v67, s34, v20
	v_med3_f32 v75, v75, s34, v20
	v_mul_f32_e32 v68, v31, v68
	v_mul_f32_e32 v76, v31, v76
	v_rndne_f32_e32 v86, v90
	v_med3_f32 v83, v83, s34, v20
	v_med3_f32 v90, v91, s34, v20
	v_mul_f32_e32 v84, v31, v84
	v_mul_f32_e32 v91, v31, v92
	v_cvt_i32_f32_e32 v33, v33
	v_cvt_i32_f32_sdwa v38, v38 dst_sel:WORD_1 dst_unused:UNUSED_PAD src0_sel:DWORD
	v_rndne_f32_e32 v35, v35
	v_med3_f32 v36, v36, s34, v20
	v_med3_f32 v44, v44, s34, v20
	v_mul_f32_e32 v37, v37, v32
	v_mul_f32_e32 v45, v32, v45
	v_cvt_i32_f32_e32 v48, v48
	v_cvt_i32_f32_sdwa v54, v54 dst_sel:WORD_1 dst_unused:UNUSED_PAD src0_sel:DWORD
	v_rndne_f32_e32 v51, v51
	v_rndne_f32_e32 v59, v59
	v_med3_f32 v52, v52, s34, v20
	v_med3_f32 v60, v60, s34, v20
	v_mul_f32_e32 v53, v32, v53
	v_mul_f32_e32 v61, v32, v61
	v_cvt_i32_f32_e32 v66, v66
	v_rndne_f32_e32 v71, v71
	v_med3_f32 v72, v72, s34, v20
; __device__ __forceinline__ unsigned pack_i8x4(float a, float b, float c, float d) {
;     const int ia = (int)rintf(fminf(fmaxf(a, -127.f), 127.f)), ib = (int)rintf(fminf(fmaxf(b, -127.f), 127.f)), ic = (int)rintf(fminf(fmaxf(c, -127.f), 127.f)), id = (int)rintf(fminf(fmaxf(d, -127.f), 127.f));
;     return (unsigned)(ia & 0xff) | ((unsigned)(ib & 0xff) << 8) | ((unsigned)(ic & 0xff) << 16) | ((unsigned)(id & 0xff) << 24);
; }
; __device__ __forceinline__ void cvt_item_i8(const float* src, int ld, int k0, int c0, unsigned char* dst, int Kd, int drow0, const float* cmx  , unsigned char* scr, int lane) {
;     const int c = lane & 7, q = lane >> 3;
;     const f32x4 cm = *(const f32x4*)(cmx + 4 * c);
;     f32x4 inv; inv[0] = cm[0] > 0.f ? 127.f / cm[0] : 0.f; inv[1] = cm[1] > 0.f ? 127.f / cm[1] : 0.f; inv[2] = cm[2] > 0.f ? 127.f / cm[2] : 0.f; inv[3] = cm[3] > 0.f ? 127.f / cm[3] : 0.f;
;     f32x4 v[4][4];
; #pragma unroll
;     for (int g = 0; g < 4; ++g)
; #pragma unroll
;         for (int j = 0; j < 4; ++j) v[g][j] = __builtin_nontemporal_load((const f32x4*)(src + (size_t)(k0 + 32 * g + 4 * q + j) * ld + c0 + 4 * c));
; #pragma unroll
;     for (int g = 0; g < 4; ++g)
; #pragma unroll
;         for (int i = 0; i < 4; ++i) *(unsigned*)(scr + (4 * c + i) * 132 + 32 * g + 4 * q) = pack_i8x4(v[g][0][i] * inv[i], v[g][1][i] * inv[i], v[g][2][i] * inv[i], v[g][3][i] * inv[i]);
	v_mul_f32_e32 v73, v32, v73
	v_cvt_i32_f32_e32 v82, v82
	v_rndne_f32_e32 v87, v87
	v_med3_f32 v88, v88, s34, v20
	v_mul_f32_e32 v89, v32, v89
	v_cvt_i32_f32_e32 v39, v39
	v_cvt_i32_f32_sdwa v43, v43 dst_sel:WORD_1 dst_unused:UNUSED_PAD src0_sel:DWORD
	v_rndne_f32_e32 v40, v40
	v_med3_f32 v41, v41, s34, v20
	v_cvt_i32_f32_e32 v55, v55
	v_rndne_f32_e32 v56, v56
	v_med3_f32 v57, v57, s34, v20
	v_rndne_f32_e32 v29, v29
	v_med3_f32 v30, v30, s34, v20
	v_mul_f32_e32 v31, v31, v96
	v_cvt_i32_f32_sdwa v42, v42 dst_sel:BYTE_3 dst_unused:UNUSED_PAD src0_sel:DWORD
	v_rndne_f32_e32 v46, v46
	v_med3_f32 v47, v47, s34, v20
	v_mul_f32_e32 v49, v32, v49
	v_cvt_i32_f32_sdwa v58, v58 dst_sel:BYTE_3 dst_unused:UNUSED_PAD src0_sel:DWORD
	v_rndne_f32_e32 v62, v62
	v_med3_f32 v63, v63, s34, v20
	v_mul_f32_e32 v65, v32, v65
	v_cvt_i32_f32_e32 v64, v64
	v_cvt_i32_f32_sdwa v70, v70 dst_sel:WORD_1 dst_unused:UNUSED_PAD src0_sel:DWORD
	v_rndne_f32_e32 v67, v67
	v_rndne_f32_e32 v75, v75
	v_med3_f32 v68, v68, s34, v20
	v_med3_f32 v76, v76, s34, v20
	v_mul_f32_e32 v69, v32, v69
	v_mul_f32_e32 v77, v32, v77
	v_cvt_i32_f32_e32 v80, v80
	v_cvt_i32_f32_sdwa v86, v86 dst_sel:WORD_1 dst_unused:UNUSED_PAD src0_sel:DWORD
	v_rndne_f32_e32 v83, v83
	v_rndne_f32_e32 v90, v90
	v_med3_f32 v84, v84, s34, v20
	v_med3_f32 v91, v91, s34, v20
	v_mul_f32_e32 v85, v32, v85
	v_mul_f32_e32 v92, v32, v93
	v_cvt_i32_f32_e32 v35, v35
	v_rndne_f32_e32 v36, v36
	v_rndne_f32_e32 v44, v44
	v_med3_f32 v37, v37, s34, v20
	v_med3_f32 v45, v45, s34, v20
	v_cvt_i32_f32_e32 v51, v51
	v_cvt_i32_f32_sdwa v59, v59 dst_sel:WORD_1 dst_unused:UNUSED_PAD src0_sel:DWORD
	v_rndne_f32_e32 v52, v52
	v_rndne_f32_e32 v60, v60
	v_med3_f32 v53, v53, s34, v20
	v_med3_f32 v61, v61, s34, v20
	v_cvt_i32_f32_e32 v71, v71
	v_rndne_f32_e32 v72, v72
	v_med3_f32 v73, v73, s34, v20
	v_cvt_i32_f32_e32 v87, v87
	v_rndne_f32_e32 v88, v88
	v_med3_f32 v89, v89, s34, v20
	v_cvt_i32_f32_e32 v40, v40
	v_rndne_f32_e32 v41, v41
	v_cvt_i32_f32_e32 v56, v56
	v_rndne_f32_e32 v57, v57
	v_cvt_i32_f32_sdwa v74, v74 dst_sel:BYTE_3 dst_unused:UNUSED_PAD src0_sel:DWORD
	v_rndne_f32_e32 v78, v78
	v_med3_f32 v79, v79, s34, v20
	v_mul_f32_e32 v81, v32, v81
	v_cvt_i32_f32_sdwa v29, v29 dst_sel:BYTE_3 dst_unused:UNUSED_PAD src0_sel:DWORD
	v_rndne_f32_e32 v30, v30
	v_med3_f32 v31, v31, s34, v20
	v_mul_f32_e32 v32, v32, v97
	v_cvt_i32_f32_sdwa v46, v46 dst_sel:BYTE_3 dst_unused:UNUSED_PAD src0_sel:DWORD
	v_rndne_f32_e32 v47, v47
	v_med3_f32 v49, v49, s34, v20
	v_cvt_i32_f32_sdwa v62, v62 dst_sel:BYTE_3 dst_unused:UNUSED_PAD src0_sel:DWORD
	v_rndne_f32_e32 v63, v63
	v_med3_f32 v65, v65, s34, v20
	v_cvt_i32_f32_e32 v67, v67
	v_cvt_i32_f32_sdwa v75, v75 dst_sel:WORD_1 dst_unused:UNUSED_PAD src0_sel:DWORD
	v_rndne_f32_e32 v68, v68
	v_rndne_f32_e32 v76, v76
	v_med3_f32 v69, v69, s34, v20
	v_med3_f32 v77, v77, s34, v20
	v_cvt_i32_f32_e32 v83, v83
	v_cvt_i32_f32_sdwa v90, v90 dst_sel:WORD_1 dst_unused:UNUSED_PAD src0_sel:DWORD
	v_rndne_f32_e32 v84, v84
	v_rndne_f32_e32 v91, v91
	v_med3_f32 v85, v85, s34, v20
	v_med3_f32 v92, v92, s34, v20
	v_cvt_i32_f32_e32 v36, v36
	v_cvt_i32_f32_sdwa v44, v44 dst_sel:WORD_1 dst_unused:UNUSED_PAD src0_sel:DWORD
	v_rndne_f32_e32 v37, v37
	v_rndne_f32_e32 v45, v45
	v_cvt_i32_f32_e32 v52, v52
	v_cvt_i32_f32_sdwa v60, v60 dst_sel:WORD_1 dst_unused:UNUSED_PAD src0_sel:DWORD
	v_rndne_f32_e32 v53, v53
	v_rndne_f32_e32 v61, v61
	v_cvt_i32_f32_e32 v72, v72
	v_rndne_f32_e32 v73, v73
	v_cvt_i32_f32_e32 v88, v88
	v_rndne_f32_e32 v89, v89
	v_cvt_i32_f32_e32 v41, v41
	v_cvt_i32_f32_e32 v57, v57
	v_cvt_i32_f32_sdwa v78, v78 dst_sel:BYTE_3 dst_unused:UNUSED_PAD src0_sel:DWORD
	v_rndne_f32_e32 v79, v79
	v_med3_f32 v81, v81, s34, v20
	v_cvt_i32_f32_sdwa v30, v30 dst_sel:BYTE_3 dst_unused:UNUSED_PAD src0_sel:DWORD
	v_rndne_f32_e32 v31, v31
	v_med3_f32 v32, v32, s34, v20
	v_cvt_i32_f32_sdwa v47, v47 dst_sel:BYTE_3 dst_unused:UNUSED_PAD src0_sel:DWORD
	v_rndne_f32_e32 v49, v49
	v_cvt_i32_f32_sdwa v63, v63 dst_sel:BYTE_3 dst_unused:UNUSED_PAD src0_sel:DWORD
	v_rndne_f32_e32 v65, v65
	v_cvt_i32_f32_e32 v68, v68
	v_cvt_i32_f32_sdwa v76, v76 dst_sel:WORD_1 dst_unused:UNUSED_PAD src0_sel:DWORD
	v_rndne_f32_e32 v69, v69
	v_rndne_f32_e32 v77, v77
	v_cvt_i32_f32_e32 v84, v84
; __device__ __forceinline__ void cvt_item_i8(const float* src, int ld, int k0, int c0, unsigned char* dst, int Kd, int drow0, const float* cmx  , unsigned char* scr, int lane) {
;     ...
;     for (int g = 0; g < 4; ++g)
; #pragma unroll
;         for (int i = 0; i < 4; ++i) *(unsigned*)(scr + (4 * c + i) * 132 + 32 * g + 4 * q) = pack_i8x4(v[g][0][i] * inv[i], v[g][1][i] * inv[i], v[g][2][i] * inv[i], v[g][3][i] * inv[i]);
;     asm volatile("s_waitcnt lgkmcnt(0)" ::: "memory");
; #pragma unroll
;     for (int r = 0; r < 4; ++r) { const int n = 8 * r + (lane >> 3), ch = lane & 7; const unsigned char* p = scr + n * 132 + ch * 16;
;         u32x4 o; o.x = *(const unsigned*)(p); o.y = *(const unsigned*)(p + 4); o.z = *(const unsigned*)(p + 8); o.w = *(const unsigned*)(p + 12);
;         *(u32x4*)(dst + (size_t)(drow0 + n) * Kd + k0 + 16 * ch) = o; }
;     asm volatile("s_waitcnt lgkmcnt(0)" ::: "memory");
	v_cvt_i32_f32_sdwa v91, v91 dst_sel:WORD_1 dst_unused:UNUSED_PAD src0_sel:DWORD
	v_rndne_f32_e32 v85, v85
	v_rndne_f32_e32 v92, v92
	v_cvt_i32_f32_e32 v37, v37
	v_cvt_i32_f32_sdwa v45, v45 dst_sel:WORD_1 dst_unused:UNUSED_PAD src0_sel:DWORD
	v_cvt_i32_f32_e32 v53, v53
	v_cvt_i32_f32_sdwa v61, v61 dst_sel:WORD_1 dst_unused:UNUSED_PAD src0_sel:DWORD
	v_cvt_i32_f32_e32 v73, v73
	v_cvt_i32_f32_e32 v89, v89
	v_lshlrev_b32_e32 v34, 8, v34
	v_lshlrev_b32_e32 v50, 8, v50
	v_cvt_i32_f32_sdwa v79, v79 dst_sel:BYTE_3 dst_unused:UNUSED_PAD src0_sel:DWORD
	v_rndne_f32_e32 v81, v81
	v_cvt_i32_f32_sdwa v31, v31 dst_sel:BYTE_3 dst_unused:UNUSED_PAD src0_sel:DWORD
	v_rndne_f32_e32 v32, v32
	v_cvt_i32_f32_sdwa v49, v49 dst_sel:BYTE_3 dst_unused:UNUSED_PAD src0_sel:DWORD
	v_cvt_i32_f32_sdwa v65, v65 dst_sel:BYTE_3 dst_unused:UNUSED_PAD src0_sel:DWORD
	v_cvt_i32_f32_e32 v69, v69
	v_cvt_i32_f32_sdwa v77, v77 dst_sel:WORD_1 dst_unused:UNUSED_PAD src0_sel:DWORD
	v_cvt_i32_f32_e32 v85, v85
	v_cvt_i32_f32_sdwa v92, v92 dst_sel:WORD_1 dst_unused:UNUSED_PAD src0_sel:DWORD
	v_and_b32_e32 v38, 0xff0000, v38
	v_and_b32_e32 v54, 0xff0000, v54
	v_lshlrev_b32_e32 v66, 8, v66
	v_lshlrev_b32_e32 v82, 8, v82
	v_perm_b32 v33, v34, v33, s35
	v_lshlrev_b32_e32 v34, 8, v39
	v_and_b32_e32 v39, 0xff0000, v43
	v_perm_b32 v43, v50, v48, s35
	v_lshlrev_b32_e32 v48, 8, v55
	v_cvt_i32_f32_sdwa v81, v81 dst_sel:BYTE_3 dst_unused:UNUSED_PAD src0_sel:DWORD
	v_cvt_i32_f32_sdwa v32, v32 dst_sel:BYTE_3 dst_unused:UNUSED_PAD src0_sel:DWORD
	v_and_b32_e32 v70, 0xff0000, v70
	v_and_b32_e32 v86, 0xff0000, v86
	v_and_b32_e32 v50, 0xff0000, v59
	v_perm_b32 v55, v66, v64, s35
	v_lshlrev_b32_e32 v59, 8, v71
	v_perm_b32 v66, v82, v80, s35
	v_lshlrev_b32_e32 v71, 8, v87
	v_or3_b32 v33, v33, v38, v42
	v_perm_b32 v34, v34, v35, s35
	v_lshlrev_b32_e32 v35, 8, v40
	v_or3_b32 v40, v43, v54, v58
	v_perm_b32 v42, v48, v51, s35
	v_lshlrev_b32_e32 v43, 8, v56
	v_and_b32_e32 v64, 0xff0000, v75
	v_and_b32_e32 v75, 0xff0000, v90
	v_and_b32_e32 v38, 0xff0000, v44
	v_and_b32_e32 v44, 0xff0000, v60
	v_or3_b32 v48, v55, v70, v74
	v_perm_b32 v51, v59, v67, s35
	v_lshlrev_b32_e32 v54, 8, v72
	v_or3_b32 v29, v66, v86, v29
	v_perm_b32 v56, v71, v83, s35
	v_lshlrev_b32_e32 v58, 8, v88
	v_or3_b32 v34, v34, v39, v46
	v_perm_b32 v35, v35, v36, s35
	v_lshlrev_b32_e32 v36, 8, v41
	ds_write2_b32 v21, v33, v40 offset1:8
	v_or3_b32 v33, v42, v50, v62
	v_perm_b32 v40, v43, v52, s35
	v_lshlrev_b32_e32 v41, 8, v57
	v_and_b32_e32 v55, 0xff0000, v76
	v_and_b32_e32 v59, 0xff0000, v91
	v_and_b32_e32 v39, 0xff0000, v45
	v_and_b32_e32 v42, 0xff0000, v61
	v_or3_b32 v43, v51, v64, v78
	v_perm_b32 v45, v54, v68, s35
	v_lshlrev_b32_e32 v46, 8, v73
	ds_write2_b32 v21, v48, v29 offset0:16 offset1:24
	v_or3_b32 v29, v56, v75, v30
	v_perm_b32 v30, v58, v84, s35
	v_lshlrev_b32_e32 v48, 8, v89
	v_or3_b32 v35, v35, v38, v47
	v_perm_b32 v36, v36, v37, s35
	ds_write2_b32 v21, v34, v33 offset0:33 offset1:41
	v_or3_b32 v33, v40, v44, v63
	v_perm_b32 v34, v41, v53, s35
	v_and_b32_e32 v50, 0xff0000, v77
	v_and_b32_e32 v51, 0xff0000, v92
	v_or3_b32 v37, v45, v55, v79
	v_perm_b32 v38, v46, v69, s35
	ds_write2_b32 v21, v43, v29 offset0:49 offset1:57
	v_or3_b32 v29, v30, v59, v31
	v_perm_b32 v30, v48, v85, s35
	v_or3_b32 v31, v36, v39, v49
	ds_write2_b32 v21, v35, v33 offset0:66 offset1:74
	v_or3_b32 v33, v34, v42, v65
	v_or3_b32 v34, v38, v50, v81
	ds_write2_b32 v21, v37, v29 offset0:82 offset1:90
	v_or3_b32 v29, v30, v51, v32
	ds_write2_b32 v21, v31, v33 offset0:99 offset1:107
	ds_write2_b32 v21, v34, v29 offset0:115 offset1:123
	s_waitcnt lgkmcnt(0)
	ds_read2_b32 v[30:31], v22 offset1:1
	ds_read2_b32 v[32:33], v22 offset0:2 offset1:3
	ds_read2_b32 v[34:35], v23 offset1:1
	ds_read2_b32 v[36:37], v24 offset1:1
	ds_read2_b32 v[38:39], v25 offset1:1
	ds_read2_b32 v[40:41], v26 offset1:1
	ds_read2_b32 v[42:43], v27 offset1:1
	ds_read2_b32 v[44:45], v28 offset1:1
	s_waitcnt lgkmcnt(6)
	global_store_dwordx4 v[10:11], v[30:33], off
	s_waitcnt lgkmcnt(4)
	global_store_dwordx4 v[12:13], v[34:37], off
	s_waitcnt lgkmcnt(2)
	global_store_dwordx4 v[14:15], v[38:41], off
	s_waitcnt lgkmcnt(0)
	global_store_dwordx4 v[6:7], v[42:45], off
	s_waitcnt lgkmcnt(0)
	s_cbranch_scc1 .LBB0_1672

; template <int GRP>
; __device__ __forceinline__ void conv_item(Frame& F, int r) {
;     ...
;     else { constexpr int KBN = (GRP == 3) ? 16 : CMS_KB, I_E = KBN * 88; const int up = r / (8 * I_E); r %= (8 * I_E); const int e = r / I_E; r %= I_E; const int kb = r / 88, nb = r % 88, n0 = nb * 32, drow = (n0 >> 7) * 256 + up * 128 + (n0 & 127);
;         if (GRP == 3) cvt_item_i8(inptr(F, up ? IN_MU : IN_MG) + (size_t)e * D * DFE, DFE, kb * 128, n0, ws + WS_MGU + (size_t)e * 2 * DFE * D, D, drow, cmx + 2 * DFF + e * 2 * DFE + drow, scr, F.lane);
; template <int L>
; __device__ __forceinline__ void layer(Frame& F, const XcdBarrier& bar, float* out, const int lo, const int hi) {
;     ...
;         if (cls == 1) { conv_all<GRP>(F, (F.G == 256) ? ((L == 0) ? SLOT_FIRST0 : SLOT_FIRST1) : 0); if (L == 0 && F.G == 256) { const int e4 = F.gw - G4_SLACK0; if (e4 >= 0 && e4 < G4_TAIL) conv_item<4>(F, 2048 + e4); } __syncthreads(); }
.LBB0_1767:
	v_readlane_b32 s0, v255, 27
	s_cmp_lg_u32 s0, 1
	s_barrier
	s_cbranch_scc1 .LBB0_1772
	s_cmpk_eq_i32 s48, 0x100
	s_cselect_b32 s0, 0x1800, 0
	v_readlane_b32 s1, v255, 10
	s_add_i32 s3, s0, s1
	s_cmpk_gt_i32 s3, 0x57ff
	v_readlane_b32 s40, v255, 13
	s_cbranch_scc1 .LBB0_1771
	v_readlane_b32 s0, v255, 9
	s_mulk_i32 s0, 0x2200
	s_add_i32 s0, s0, 0
	v_and_b32_e32 v2, 7, v0
	s_add_u32 s4, s50, 0x8200000
	v_lshrrev_b32_e32 v1, 3, v194
	v_lshlrev_b32_e32 v4, 2, v2
	v_mul_u32_u24_e32 v7, 0x210, v2
	v_lshlrev_b32_e32 v2, 4, v2
	s_addc_u32 s12, s51, 0
	v_lshlrev_b32_e32 v16, 2, v1
	v_add_u32_e32 v8, s0, v2
	v_mul_u32_u24_e32 v9, 0x84, v1
	s_add_u32 s13, s50, 0x8b000
	v_mov_b32_e32 v3, 0
	v_add_u32_e32 v6, s0, v16
	v_add_u32_e32 v22, v8, v9
	s_addc_u32 s14, s51, 0
	v_or_b32_e32 v17, 8, v1
	v_or_b32_e32 v18, 16, v1
	v_or_b32_e32 v19, 24, v1
	s_movk_i32 s15, 0xa0
	v_lshlrev_b32_e32 v4, 2, v4
	v_mov_b32_e32 v5, v3
	s_mov_b32 s16, 0x42fe0000
	s_movk_i32 s17, 0x2000
	s_movk_i32 s18, 0x5000
	s_mov_b32 s19, 0x8000
	s_mov_b32 s20, 0x58000
	s_mov_b32 s21, 0x5a000
	s_mov_b32 s22, 0x5d000
	s_mov_b32 s23, 0x60000
	s_mov_b32 s24, 0xb0000
	s_mov_b32 s25, 0xb2000
	s_mov_b32 s26, 0xb5000
	s_mov_b32 s27, 0xb8000
	s_mov_b32 s28, 0x108000
	s_mov_b32 s29, 0x10a000
	s_mov_b32 s30, 0x10d000
	s_mov_b32 s31, 0x110000
	s_mov_b32 s34, 0xc2fe0000
	v_mov_b32_e32 v20, 0x42fe0000
	s_mov_b32 s35, 0xc0c0500
	v_add_u32_e32 v21, v6, v7
	v_add_u32_e32 v23, 0x420, v22
	v_add_u32_e32 v24, 0x428, v22
	v_add_u32_e32 v25, 0x840, v22
	v_add_u32_e32 v26, 0x848, v22
	v_add_u32_e32 v27, 0xc60, v22
	v_add_u32_e32 v28, 0xc68, v22
	v_readlane_b32 s0, v255, 9
	s_cmp_lt_u32 s0, 4
	s_cbranch_scc1 .Lstg_1770
	s_sleep 44

; __device__ __forceinline__ void cvt_item_i8(const float* src, int ld, int k0, int c0, unsigned char* dst, int Kd, int drow0, const float* cmx  , unsigned char* scr, int lane) {
;     const int c = lane & 7, q = lane >> 3;
;     const f32x4 cm = *(const f32x4*)(cmx + 4 * c);
;     f32x4 inv; inv[0] = cm[0] > 0.f ? 127.f / cm[0] : 0.f; inv[1] = cm[1] > 0.f ? 127.f / cm[1] : 0.f; inv[2] = cm[2] > 0.f ? 127.f / cm[2] : 0.f; inv[3] = cm[3] > 0.f ? 127.f / cm[3] : 0.f;
;     f32x4 v[4][4];
; #pragma unroll
;     for (int g = 0; g < 4; ++g)
; #pragma unroll
;         for (int j = 0; j < 4; ++j) v[g][j] = __builtin_nontemporal_load((const f32x4*)(src + (size_t)(k0 + 32 * g + 4 * q + j) * ld + c0 + 4 * c));
; template <int GRP>
; __device__ __forceinline__ void conv_item(Frame& F, int r) {
;     ...
;     else { constexpr int KBN = (GRP == 3) ? 16 : CMS_KB, I_E = KBN * 88; const int up = r / (8 * I_E); r %= (8 * I_E); const int e = r / I_E; r %= I_E; const int kb = r / 88, nb = r % 88, n0 = nb * 32, drow = (n0 >> 7) * 256 + up * 128 + (n0 & 127);
;         if (GRP == 3) cvt_item_i8(inptr(F, up ? IN_MU : IN_MG) + (size_t)e * D * DFE, DFE, kb * 128, n0, ws + WS_MGU + (size_t)e * 2 * DFE * D, D, drow, cmx + 2 * DFF + e * 2 * DFE + drow, scr, F.lane);
;         else colmax_item(inptr(F, up ? IN_MU : IN_MG) + (size_t)e * D * DFE, DFE, kb * 128, n0, cmx + 2 * DFF + e * 2 * DFE + drow, F.lane); }
.LBB0_1906:
	v_readlane_b32 s0, v255, 27
	s_cmp_lg_u32 s0, 2
	s_barrier
	s_cbranch_scc1 .LBB0_1911
	s_cmpk_eq_i32 s48, 0x100
	s_cselect_b32 s0, 0x1800, 0
	v_readlane_b32 s1, v255, 10
	s_add_i32 s3, s0, s1
	s_cmpk_gt_i32 s3, 0x57ff
	v_readlane_b32 s42, v255, 13
	s_cbranch_scc1 .LBB0_1910
	v_readlane_b32 s0, v255, 9
	s_mulk_i32 s0, 0x2200
	s_add_i32 s0, s0, 0
	v_and_b32_e32 v2, 7, v0
	s_add_u32 s4, s50, 0x8200000
	s_waitcnt vmcnt(5)
	v_lshrrev_b32_e32 v1, 3, v194
	v_lshlrev_b32_e32 v4, 2, v2
	v_mul_u32_u24_e32 v7, 0x210, v2
	v_lshlrev_b32_e32 v2, 4, v2
	s_addc_u32 s12, s51, 0
	v_lshlrev_b32_e32 v16, 2, v1
	v_add_u32_e32 v8, s0, v2
	v_mul_u32_u24_e32 v9, 0x84, v1
	s_add_u32 s13, s50, 0x8b000
	v_mov_b32_e32 v3, 0
	v_add_u32_e32 v6, s0, v16
	v_add_u32_e32 v22, v8, v9
	s_addc_u32 s14, s51, 0
	v_or_b32_e32 v17, 8, v1
	v_or_b32_e32 v18, 16, v1
	v_or_b32_e32 v19, 24, v1
	s_movk_i32 s15, 0xa0
	v_lshlrev_b32_e32 v4, 2, v4
	v_mov_b32_e32 v5, v3
	s_mov_b32 s16, 0x42fe0000
	s_movk_i32 s17, 0x2000
	s_movk_i32 s20, 0x5000
	s_mov_b32 s21, 0x8000
	s_mov_b32 s22, 0x58000
	s_mov_b32 s23, 0x5a000
	s_mov_b32 s24, 0x5d000
	s_mov_b32 s25, 0x60000
	s_mov_b32 s26, 0xb0000
	s_mov_b32 s27, 0xb2000
	s_mov_b32 s28, 0xb5000
	s_mov_b32 s29, 0xb8000
	s_mov_b32 s30, 0x108000
	s_mov_b32 s31, 0x10a000
	s_mov_b32 s34, 0x10d000
	s_mov_b32 s35, 0x110000
	s_mov_b32 s36, 0xc2fe0000
	v_mov_b32_e32 v20, 0x42fe0000
	s_mov_b32 s37, 0xc0c0500
	v_add_u32_e32 v21, v6, v7
	v_add_u32_e32 v23, 0x420, v22
	v_add_u32_e32 v24, 0x428, v22
	v_add_u32_e32 v25, 0x840, v22
	v_add_u32_e32 v26, 0x848, v22
	v_add_u32_e32 v27, 0xc60, v22
	v_add_u32_e32 v28, 0xc68, v22
	v_readlane_b32 s0, v255, 9
	s_cmp_lt_u32 s0, 4
	s_cbranch_scc1 .Lstg_1909
	s_sleep 44
.Lstg_1909:
.LBB0_1909:
	s_mul_hi_i32 s0, s3, 0x2e8ba2e9
	s_lshr_b32 s1, s0, 31
	s_ashr_i32 s0, s0, 11
	s_add_i32 s0, s0, s1
	s_mul_i32 s1, s0, 0xffffd400
	s_lshl_b32 s6, s0, 7
	s_add_i32 s0, s3, s1
	s_mul_i32 s1, s0, 0xba3
	s_lshr_b32 s7, s1, 31
	s_ashr_i32 s1, s1, 22
	s_add_i32 s1, s1, s7
	s_mul_i32 s7, s1, 0x580
	s_sub_i32 s0, s0, s7
	s_sext_i32_i16 s38, s0
	s_mulk_i32 s38, 0xba3
	s_lshr_b32 s40, s38, 31
	s_ashr_i32 s38, s38, 18
	s_add_i32 s40, s38, s40
	s_sext_i32_i16 s38, s40
	s_mulk_i32 s40, 0x58
	s_sub_i32 s0, s0, s40
	s_sext_i32_i16 s40, s0
	s_lshl_b32 s0, s40, 5
	s_lshl_b32 s40, s40, 6
	s_and_b32 s40, s40, 0xffffff00
	s_and_b32 s41, s0, 0x60
	s_add_i32 s40, s40, s6
	s_add_i32 s39, s3, 0x2bff
	s_or_b32 s6, s40, s41
	s_cmpk_lt_u32 s39, 0x57ff
	s_cselect_b32 s39, s15, 0xa8
	v_or_b32_e32 v8, s6, v17
	s_add_i32 s39, s39, 0
	v_ashrrev_i32_e32 v9, 31, v8
	s_add_i32 s39, s39, 0x20200
	v_lshlrev_b64 v[98:99], 11, v[8:9]
	v_mov_b32_e32 v8, s39
	ds_read_b64 v[8:9], v8
	s_sext_i32_i16 s11, s1
	s_mul_i32 s9, s11, 0x1600000
	s_mul_hi_i32 s1, s11, 0x1600000
	s_mul_i32 s10, s11, 0xb00000
	s_waitcnt lgkmcnt(0)
	v_readfirstlane_b32 s39, v8
	v_readfirstlane_b32 s40, v9
	s_add_u32 s9, s39, s9
	s_addc_u32 s39, s40, s1
	s_lshl_b32 s38, s38, 7
	s_mul_hi_i32 s7, s11, 0xb00000
	s_add_u32 s10, s4, s10
	s_mul_hi_i32 s8, s11, 0x5800
	s_mulk_i32 s11, 0x5800
	s_addc_u32 s40, s12, s7
	s_add_u32 s1, s13, s11
	s_addc_u32 s8, s14, s8
	s_ashr_i32 s7, s6, 31
	v_or_b32_e32 v6, s6, v1
	v_or_b32_e32 v10, s6, v18
	v_or_b32_e32 v12, s6, v19
	s_lshl_b64 s[6:7], s[6:7], 2
	s_add_u32 s6, s1, s6
	s_addc_u32 s7, s8, s7
	s_ashr_i32 s1, s0, 31
	s_lshl_b64 s[0:1], s[0:1], 2
	v_or_b32_e32 v8, s38, v16
	s_add_u32 s0, s9, s0
	v_ashrrev_i32_e32 v11, 31, v10
	v_mul_i32_i24_e32 v8, 0x2c00, v8
	s_addc_u32 s1, s39, s1
	v_lshlrev_b64 v[100:101], 11, v[10:11]
	v_ashrrev_i32_e32 v9, 31, v8
	v_lshl_add_u64 v[10:11], s[0:1], 0, v[4:5]
	v_ashrrev_i32_e32 v7, 31, v6
	v_ashrrev_i32_e32 v13, 31, v12
	v_lshl_add_u64 v[10:11], v[10:11], 0, v[8:9]
	v_lshlrev_b64 v[14:15], 11, v[6:7]
	v_lshlrev_b64 v[6:7], 11, v[12:13]
	v_add_co_u32_e32 v12, vcc, s17, v10
	global_load_dwordx4 v[30:33], v4, s[6:7]
	s_nop 0
	v_addc_co_u32_e32 v13, vcc, 0, v11, vcc
	v_add_co_u32_e32 v42, vcc, s20, v10
	s_ashr_i32 s6, s38, 31
	s_nop 0
	v_addc_co_u32_e32 v43, vcc, 0, v11, vcc
	v_add_co_u32_e32 v46, vcc, s21, v10
	s_add_u32 s0, s10, s38
	s_nop 0
	v_addc_co_u32_e32 v47, vcc, 0, v11, vcc
	v_add_co_u32_e32 v50, vcc, s22, v10
	s_addc_u32 s1, s40, s6
	s_nop 0
	v_addc_co_u32_e32 v51, vcc, 0, v11, vcc
	v_add_co_u32_e32 v54, vcc, s23, v10
	v_lshl_add_u64 v[8:9], s[0:1], 0, v[2:3]
	s_nop 0
	v_addc_co_u32_e32 v55, vcc, 0, v11, vcc
	v_add_co_u32_e32 v58, vcc, s24, v10
	v_lshl_add_u64 v[6:7], v[8:9], 0, v[6:7]
	s_nop 0
	v_addc_co_u32_e32 v59, vcc, 0, v11, vcc
	v_add_co_u32_e32 v62, vcc, s25, v10
	s_add_i32 s3, s3, s42
	s_nop 0
	v_addc_co_u32_e32 v63, vcc, 0, v11, vcc
	v_add_co_u32_e32 v66, vcc, s26, v10
	s_cmpk_lt_i32 s3, 0x5800
	s_nop 0
	v_addc_co_u32_e32 v67, vcc, 0, v11, vcc
	v_add_co_u32_e32 v70, vcc, s27, v10
	s_nop 0
	s_nop 0
	v_addc_co_u32_e32 v71, vcc, 0, v11, vcc
	v_add_co_u32_e32 v74, vcc, s28, v10
	s_nop 0
	s_nop 0
	v_addc_co_u32_e32 v75, vcc, 0, v11, vcc
	v_add_co_u32_e32 v78, vcc, s29, v10
	s_nop 0
	s_nop 0
	v_addc_co_u32_e32 v79, vcc, 0, v11, vcc
	v_add_co_u32_e32 v82, vcc, s30, v10
	s_nop 0
	s_nop 0
	v_addc_co_u32_e32 v83, vcc, 0, v11, vcc
	v_add_co_u32_e32 v86, vcc, s31, v10
	s_nop 0
	s_nop 0
	v_addc_co_u32_e32 v87, vcc, 0, v11, vcc
	v_add_co_u32_e32 v90, vcc, s34, v10
	s_nop 0
	s_nop 0
	v_addc_co_u32_e32 v91, vcc, 0, v11, vcc
	v_add_co_u32_e32 v94, vcc, s35, v10
	s_nop 0
	s_nop 0
	v_addc_co_u32_e32 v95, vcc, 0, v11, vcc
	global_load_dwordx4 v[34:37], v[10:11], off nt
	global_load_dwordx4 v[38:41], v[12:13], off offset:3072 nt
	s_nop 0
	global_load_dwordx4 v[42:45], v[42:43], off offset:2048 nt
	s_nop 0
	global_load_dwordx4 v[46:49], v[46:47], off offset:1024 nt
	s_nop 0
	global_load_dwordx4 v[50:53], v[50:51], off nt
	s_nop 0
	global_load_dwordx4 v[54:57], v[54:55], off offset:3072 nt
	s_nop 0
	global_load_dwordx4 v[58:61], v[58:59], off offset:2048 nt
	s_nop 0
	global_load_dwordx4 v[62:65], v[62:63], off offset:1024 nt
	s_nop 0
	global_load_dwordx4 v[66:69], v[66:67], off nt
	s_nop 0
	global_load_dwordx4 v[70:73], v[70:71], off offset:3072 nt
	s_nop 0
	global_load_dwordx4 v[74:77], v[74:75], off offset:2048 nt
	s_nop 0
	global_load_dwordx4 v[78:81], v[78:79], off offset:1024 nt
	s_nop 0
	global_load_dwordx4 v[82:85], v[82:83], off nt
	s_nop 0
	global_load_dwordx4 v[86:89], v[86:87], off offset:3072 nt
	s_nop 0
	global_load_dwordx4 v[90:93], v[90:91], off offset:2048 nt
	s_nop 0
	global_load_dwordx4 v[94:97], v[94:95], off offset:1024 nt
	s_waitcnt vmcnt(16)
; __device__ __forceinline__ unsigned pack_i8x4(float a, float b, float c, float d) {
;     const int ia = (int)rintf(fminf(fmaxf(a, -127.f), 127.f)), ib = (int)rintf(fminf(fmaxf(b, -127.f), 127.f)), ic = (int)rintf(fminf(fmaxf(c, -127.f), 127.f)), id = (int)rintf(fminf(fmaxf(d, -127.f), 127.f));
;     return (unsigned)(ia & 0xff) | ((unsigned)(ib & 0xff) << 8) | ((unsigned)(ic & 0xff) << 16) | ((unsigned)(id & 0xff) << 24);
; }
; __device__ __forceinline__ void cvt_item_i8(const float* src, int ld, int k0, int c0, unsigned char* dst, int Kd, int drow0, const float* cmx  , unsigned char* scr, int lane) {
;     const int c = lane & 7, q = lane >> 3;
;     const f32x4 cm = *(const f32x4*)(cmx + 4 * c);
;     f32x4 inv; inv[0] = cm[0] > 0.f ? 127.f / cm[0] : 0.f; inv[1] = cm[1] > 0.f ? 127.f / cm[1] : 0.f; inv[2] = cm[2] > 0.f ? 127.f / cm[2] : 0.f; inv[3] = cm[3] > 0.f ? 127.f / cm[3] : 0.f;
;     f32x4 v[4][4];
; #pragma unroll
;     for (int g = 0; g < 4; ++g)
; #pragma unroll
;         for (int j = 0; j < 4; ++j) v[g][j] = __builtin_nontemporal_load((const f32x4*)(src + (size_t)(k0 + 32 * g + 4 * q + j) * ld + c0 + 4 * c));
; #pragma unroll
;     for (int g = 0; g < 4; ++g)
; #pragma unroll
;         for (int i = 0; i < 4; ++i) *(unsigned*)(scr + (4 * c + i) * 132 + 32 * g + 4 * q) = pack_i8x4(v[g][0][i] * inv[i], v[g][1][i] * inv[i], v[g][2][i] * inv[i], v[g][3][i] * inv[i]);
	v_div_scale_f32 v29, s[0:1], v30, v30, s16
	v_rcp_f32_e32 v105, v29
	v_div_scale_f32 v103, s[0:1], v33, v33, s16
	v_fma_f32 v109, -v29, v105, 1.0
	v_rcp_f32_e32 v108, v103
	v_fmac_f32_e32 v105, v109, v105
	v_div_scale_f32 v102, s[8:9], s16, v32, s16
	v_lshl_add_u64 v[12:13], v[8:9], 0, v[98:99]
	v_div_scale_f32 v99, s[0:1], v31, v31, s16
	v_rcp_f32_e32 v106, v99
	v_lshl_add_u64 v[10:11], v[8:9], 0, v[14:15]
	v_lshl_add_u64 v[14:15], v[8:9], 0, v[100:101]
	v_div_scale_f32 v101, s[0:1], v32, v32, s16
	v_rcp_f32_e32 v107, v101
	v_div_scale_f32 v98, vcc, s16, v30, s16
	v_fma_f32 v110, -v99, v106, 1.0
	v_div_scale_f32 v100, s[6:7], s16, v31, s16
	v_fmac_f32_e32 v106, v110, v106
	v_mul_f32_e32 v109, v98, v105
	v_fma_f32 v111, -v101, v107, 1.0
	v_mul_f32_e32 v110, v100, v106
	v_fma_f32 v113, -v29, v109, v98
	v_fmac_f32_e32 v107, v111, v107
	v_fma_f32 v114, -v99, v110, v100
	v_fmac_f32_e32 v109, v113, v105
	v_fma_f32 v112, -v103, v108, 1.0
	v_mul_f32_e32 v111, v102, v107
	v_fmac_f32_e32 v110, v114, v106
	v_fma_f32 v29, -v29, v109, v98
	v_div_scale_f32 v104, s[10:11], s16, v33, s16
	v_fmac_f32_e32 v108, v112, v108
	v_fma_f32 v115, -v101, v111, v102
	v_fma_f32 v98, -v99, v110, v100
	v_div_fmas_f32 v29, v29, v105, v109
	s_mov_b64 vcc, s[6:7]
	v_mul_f32_e32 v112, v104, v108
	v_fmac_f32_e32 v111, v115, v107
	v_div_fixup_f32 v29, v29, v30, s16
	v_div_fmas_f32 v98, v98, v106, v110
	v_cmp_lt_f32_e32 vcc, 0, v30
	v_fma_f32 v116, -v103, v112, v104
	v_fma_f32 v99, -v101, v111, v102
	v_cndmask_b32_e32 v29, 0, v29, vcc
	s_mov_b64 vcc, s[8:9]
	v_fmac_f32_e32 v112, v116, v108
	v_div_fixup_f32 v30, v98, v31, s16
	v_div_fmas_f32 v98, v99, v107, v111
	v_cmp_lt_f32_e32 vcc, 0, v31
	v_fma_f32 v100, -v103, v112, v104
	v_div_fixup_f32 v31, v98, v32, s16
	v_cndmask_b32_e32 v30, 0, v30, vcc
	s_mov_b64 vcc, s[10:11]
	v_div_fmas_f32 v98, v100, v108, v112
	v_cmp_lt_f32_e32 vcc, 0, v32
	v_div_fixup_f32 v32, v98, v33, s16
	s_waitcnt vmcnt(0) lgkmcnt(0)
	v_mul_f32_e32 v34, v34, v29
	v_mul_f32_e32 v38, v29, v38
	v_mul_f32_e32 v42, v29, v42
	v_mul_f32_e32 v46, v29, v46
	v_mul_f32_e32 v50, v29, v50
	v_mul_f32_e32 v54, v29, v54
	v_mul_f32_e32 v58, v29, v58
	v_mul_f32_e32 v62, v29, v62
	v_mul_f32_e32 v66, v29, v66
	v_mul_f32_e32 v70, v29, v70
	v_mul_f32_e32 v74, v29, v74
	v_mul_f32_e32 v78, v29, v78
	v_mul_f32_e32 v82, v29, v82
	v_mul_f32_e32 v86, v29, v86
	v_cndmask_b32_e32 v31, 0, v31, vcc
	v_med3_f32 v34, v34, s36, v20
	v_med3_f32 v38, v38, s36, v20
	v_med3_f32 v42, v42, s36, v20
	v_med3_f32 v46, v46, s36, v20
	v_mul_f32_e32 v39, v30, v39
	v_mul_f32_e32 v43, v30, v43
	v_mul_f32_e32 v47, v30, v47
	v_med3_f32 v50, v50, s36, v20
	v_med3_f32 v54, v54, s36, v20
	v_mul_f32_e32 v55, v30, v55
	v_cmp_lt_f32_e32 vcc, 0, v33
	v_mul_f32_e32 v90, v29, v90
	v_mul_f32_e32 v35, v35, v30
	v_med3_f32 v58, v58, s36, v20
	v_med3_f32 v62, v62, s36, v20
	v_mul_f32_e32 v51, v30, v51
	v_mul_f32_e32 v59, v30, v59
	v_mul_f32_e32 v63, v30, v63
	v_med3_f32 v66, v66, s36, v20
	v_med3_f32 v70, v70, s36, v20
	v_med3_f32 v74, v74, s36, v20
	v_med3_f32 v78, v78, s36, v20
	v_mul_f32_e32 v71, v30, v71
	v_mul_f32_e32 v79, v30, v79
	v_med3_f32 v82, v82, s36, v20
	v_med3_f32 v86, v86, s36, v20
	v_mul_f32_e32 v87, v30, v87
	v_cndmask_b32_e32 v32, 0, v32, vcc
	v_rndne_f32_e32 v33, v34
	v_rndne_f32_e32 v34, v38
	v_rndne_f32_e32 v38, v42
	v_rndne_f32_e32 v42, v46
	v_med3_f32 v39, v39, s36, v20
	v_med3_f32 v43, v43, s36, v20
	v_med3_f32 v46, v47, s36, v20
	v_mul_f32_e32 v40, v31, v40
	v_mul_f32_e32 v47, v31, v48
	v_rndne_f32_e32 v48, v50
	v_rndne_f32_e32 v50, v54
	v_med3_f32 v55, v55, s36, v20
	v_mul_f32_e32 v56, v31, v56
	v_mul_f32_e32 v29, v29, v94
	v_mul_f32_e32 v67, v30, v67
	v_mul_f32_e32 v75, v30, v75
	v_med3_f32 v90, v90, s36, v20
	v_mul_f32_e32 v83, v30, v83
	v_mul_f32_e32 v91, v30, v91
	v_med3_f32 v35, v35, s36, v20
	v_mul_f32_e32 v36, v36, v31
	v_mul_f32_e32 v44, v31, v44
	v_rndne_f32_e32 v54, v58
	v_rndne_f32_e32 v58, v62
	v_med3_f32 v51, v51, s36, v20
	v_med3_f32 v59, v59, s36, v20
	v_med3_f32 v62, v63, s36, v20
	v_mul_f32_e32 v52, v31, v52
	v_mul_f32_e32 v60, v31, v60
	v_mul_f32_e32 v63, v31, v64
	v_rndne_f32_e32 v64, v66
	v_rndne_f32_e32 v66, v70
	v_rndne_f32_e32 v70, v74
	v_rndne_f32_e32 v74, v78
	v_med3_f32 v71, v71, s36, v20
	v_med3_f32 v78, v79, s36, v20
	v_mul_f32_e32 v72, v31, v72
	v_mul_f32_e32 v79, v31, v80
	v_rndne_f32_e32 v80, v82
	v_rndne_f32_e32 v82, v86
	v_med3_f32 v87, v87, s36, v20
	v_mul_f32_e32 v88, v31, v88
	v_cvt_i32_f32_e32 v34, v34
	v_rndne_f32_e32 v39, v39
	v_rndne_f32_e32 v43, v43
	v_med3_f32 v40, v40, s36, v20
	v_mul_f32_e32 v41, v32, v41
	v_cvt_i32_f32_e32 v50, v50
	v_rndne_f32_e32 v55, v55
	v_med3_f32 v56, v56, s36, v20
	v_mul_f32_e32 v57, v32, v57
	v_med3_f32 v29, v29, s36, v20
	v_mul_f32_e32 v30, v30, v95
	v_med3_f32 v67, v67, s36, v20
	v_med3_f32 v75, v75, s36, v20
	v_mul_f32_e32 v68, v31, v68
	v_mul_f32_e32 v76, v31, v76
	v_rndne_f32_e32 v86, v90
	v_med3_f32 v83, v83, s36, v20
	v_med3_f32 v90, v91, s36, v20
	v_mul_f32_e32 v84, v31, v84
	v_mul_f32_e32 v91, v31, v92
	v_cvt_i32_f32_e32 v33, v33
	v_cvt_i32_f32_sdwa v38, v38 dst_sel:WORD_1 dst_unused:UNUSED_PAD src0_sel:DWORD
	v_rndne_f32_e32 v35, v35
	v_med3_f32 v36, v36, s36, v20
	v_med3_f32 v44, v44, s36, v20
	v_mul_f32_e32 v37, v37, v32
	v_mul_f32_e32 v45, v32, v45
	v_cvt_i32_f32_e32 v48, v48
	v_cvt_i32_f32_sdwa v54, v54 dst_sel:WORD_1 dst_unused:UNUSED_PAD src0_sel:DWORD
	v_rndne_f32_e32 v51, v51
	v_rndne_f32_e32 v59, v59
	v_med3_f32 v52, v52, s36, v20
	v_med3_f32 v60, v60, s36, v20
	v_mul_f32_e32 v53, v32, v53
	v_mul_f32_e32 v61, v32, v61
	v_cvt_i32_f32_e32 v66, v66
	v_rndne_f32_e32 v71, v71
	v_med3_f32 v72, v72, s36, v20
; __device__ __forceinline__ unsigned pack_i8x4(float a, float b, float c, float d) {
;     const int ia = (int)rintf(fminf(fmaxf(a, -127.f), 127.f)), ib = (int)rintf(fminf(fmaxf(b, -127.f), 127.f)), ic = (int)rintf(fminf(fmaxf(c, -127.f), 127.f)), id = (int)rintf(fminf(fmaxf(d, -127.f), 127.f));
;     return (unsigned)(ia & 0xff) | ((unsigned)(ib & 0xff) << 8) | ((unsigned)(ic & 0xff) << 16) | ((unsigned)(id & 0xff) << 24);
; }
; __device__ __forceinline__ void cvt_item_i8(const float* src, int ld, int k0, int c0, unsigned char* dst, int Kd, int drow0, const float* cmx  , unsigned char* scr, int lane) {
;     const int c = lane & 7, q = lane >> 3;
;     const f32x4 cm = *(const f32x4*)(cmx + 4 * c);
;     f32x4 inv; inv[0] = cm[0] > 0.f ? 127.f / cm[0] : 0.f; inv[1] = cm[1] > 0.f ? 127.f / cm[1] : 0.f; inv[2] = cm[2] > 0.f ? 127.f / cm[2] : 0.f; inv[3] = cm[3] > 0.f ? 127.f / cm[3] : 0.f;
;     f32x4 v[4][4];
; #pragma unroll
;     for (int g = 0; g < 4; ++g)
; #pragma unroll
;         for (int j = 0; j < 4; ++j) v[g][j] = __builtin_nontemporal_load((const f32x4*)(src + (size_t)(k0 + 32 * g + 4 * q + j) * ld + c0 + 4 * c));
; #pragma unroll
;     for (int g = 0; g < 4; ++g)
; #pragma unroll
;         for (int i = 0; i < 4; ++i) *(unsigned*)(scr + (4 * c + i) * 132 + 32 * g + 4 * q) = pack_i8x4(v[g][0][i] * inv[i], v[g][1][i] * inv[i], v[g][2][i] * inv[i], v[g][3][i] * inv[i]);
	v_mul_f32_e32 v73, v32, v73
	v_cvt_i32_f32_e32 v82, v82
	v_rndne_f32_e32 v87, v87
	v_med3_f32 v88, v88, s36, v20
	v_mul_f32_e32 v89, v32, v89
	v_cvt_i32_f32_e32 v39, v39
	v_cvt_i32_f32_sdwa v43, v43 dst_sel:WORD_1 dst_unused:UNUSED_PAD src0_sel:DWORD
	v_rndne_f32_e32 v40, v40
	v_med3_f32 v41, v41, s36, v20
	v_cvt_i32_f32_e32 v55, v55
	v_rndne_f32_e32 v56, v56
	v_med3_f32 v57, v57, s36, v20
	v_rndne_f32_e32 v29, v29
	v_med3_f32 v30, v30, s36, v20
	v_mul_f32_e32 v31, v31, v96
	v_cvt_i32_f32_sdwa v42, v42 dst_sel:BYTE_3 dst_unused:UNUSED_PAD src0_sel:DWORD
	v_rndne_f32_e32 v46, v46
	v_med3_f32 v47, v47, s36, v20
	v_mul_f32_e32 v49, v32, v49
	v_cvt_i32_f32_sdwa v58, v58 dst_sel:BYTE_3 dst_unused:UNUSED_PAD src0_sel:DWORD
	v_rndne_f32_e32 v62, v62
	v_med3_f32 v63, v63, s36, v20
	v_mul_f32_e32 v65, v32, v65
	v_cvt_i32_f32_e32 v64, v64
	v_cvt_i32_f32_sdwa v70, v70 dst_sel:WORD_1 dst_unused:UNUSED_PAD src0_sel:DWORD
	v_rndne_f32_e32 v67, v67
	v_rndne_f32_e32 v75, v75
	v_med3_f32 v68, v68, s36, v20
	v_med3_f32 v76, v76, s36, v20
	v_mul_f32_e32 v69, v32, v69
	v_mul_f32_e32 v77, v32, v77
	v_cvt_i32_f32_e32 v80, v80
	v_cvt_i32_f32_sdwa v86, v86 dst_sel:WORD_1 dst_unused:UNUSED_PAD src0_sel:DWORD
	v_rndne_f32_e32 v83, v83
	v_rndne_f32_e32 v90, v90
	v_med3_f32 v84, v84, s36, v20
	v_med3_f32 v91, v91, s36, v20
	v_mul_f32_e32 v85, v32, v85
	v_mul_f32_e32 v92, v32, v93
	v_cvt_i32_f32_e32 v35, v35
	v_rndne_f32_e32 v36, v36
	v_rndne_f32_e32 v44, v44
	v_med3_f32 v37, v37, s36, v20
	v_med3_f32 v45, v45, s36, v20
	v_cvt_i32_f32_e32 v51, v51
	v_cvt_i32_f32_sdwa v59, v59 dst_sel:WORD_1 dst_unused:UNUSED_PAD src0_sel:DWORD
	v_rndne_f32_e32 v52, v52
	v_rndne_f32_e32 v60, v60
	v_med3_f32 v53, v53, s36, v20
	v_med3_f32 v61, v61, s36, v20
	v_cvt_i32_f32_e32 v71, v71
	v_rndne_f32_e32 v72, v72
	v_med3_f32 v73, v73, s36, v20
	v_cvt_i32_f32_e32 v87, v87
	v_rndne_f32_e32 v88, v88
	v_med3_f32 v89, v89, s36, v20
	v_cvt_i32_f32_e32 v40, v40
	v_rndne_f32_e32 v41, v41
	v_cvt_i32_f32_e32 v56, v56
	v_rndne_f32_e32 v57, v57
	v_cvt_i32_f32_sdwa v74, v74 dst_sel:BYTE_3 dst_unused:UNUSED_PAD src0_sel:DWORD
	v_rndne_f32_e32 v78, v78
	v_med3_f32 v79, v79, s36, v20
	v_mul_f32_e32 v81, v32, v81
	v_cvt_i32_f32_sdwa v29, v29 dst_sel:BYTE_3 dst_unused:UNUSED_PAD src0_sel:DWORD
	v_rndne_f32_e32 v30, v30
	v_med3_f32 v31, v31, s36, v20
	v_mul_f32_e32 v32, v32, v97
	v_cvt_i32_f32_sdwa v46, v46 dst_sel:BYTE_3 dst_unused:UNUSED_PAD src0_sel:DWORD
	v_rndne_f32_e32 v47, v47
	v_med3_f32 v49, v49, s36, v20
	v_cvt_i32_f32_sdwa v62, v62 dst_sel:BYTE_3 dst_unused:UNUSED_PAD src0_sel:DWORD
	v_rndne_f32_e32 v63, v63
	v_med3_f32 v65, v65, s36, v20
	v_cvt_i32_f32_e32 v67, v67
	v_cvt_i32_f32_sdwa v75, v75 dst_sel:WORD_1 dst_unused:UNUSED_PAD src0_sel:DWORD
	v_rndne_f32_e32 v68, v68
	v_rndne_f32_e32 v76, v76
	v_med3_f32 v69, v69, s36, v20
	v_med3_f32 v77, v77, s36, v20
	v_cvt_i32_f32_e32 v83, v83
	v_cvt_i32_f32_sdwa v90, v90 dst_sel:WORD_1 dst_unused:UNUSED_PAD src0_sel:DWORD
	v_rndne_f32_e32 v84, v84
	v_rndne_f32_e32 v91, v91
	v_med3_f32 v85, v85, s36, v20
	v_med3_f32 v92, v92, s36, v20
	v_cvt_i32_f32_e32 v36, v36
	v_cvt_i32_f32_sdwa v44, v44 dst_sel:WORD_1 dst_unused:UNUSED_PAD src0_sel:DWORD
	v_rndne_f32_e32 v37, v37
	v_rndne_f32_e32 v45, v45
	v_cvt_i32_f32_e32 v52, v52
	v_cvt_i32_f32_sdwa v60, v60 dst_sel:WORD_1 dst_unused:UNUSED_PAD src0_sel:DWORD
	v_rndne_f32_e32 v53, v53
	v_rndne_f32_e32 v61, v61
	v_cvt_i32_f32_e32 v72, v72
	v_rndne_f32_e32 v73, v73
	v_cvt_i32_f32_e32 v88, v88
	v_rndne_f32_e32 v89, v89
	v_cvt_i32_f32_e32 v41, v41
	v_cvt_i32_f32_e32 v57, v57
	v_cvt_i32_f32_sdwa v78, v78 dst_sel:BYTE_3 dst_unused:UNUSED_PAD src0_sel:DWORD
	v_rndne_f32_e32 v79, v79
	v_med3_f32 v81, v81, s36, v20
	v_cvt_i32_f32_sdwa v30, v30 dst_sel:BYTE_3 dst_unused:UNUSED_PAD src0_sel:DWORD
	v_rndne_f32_e32 v31, v31
	v_med3_f32 v32, v32, s36, v20
	v_cvt_i32_f32_sdwa v47, v47 dst_sel:BYTE_3 dst_unused:UNUSED_PAD src0_sel:DWORD
	v_rndne_f32_e32 v49, v49
	v_cvt_i32_f32_sdwa v63, v63 dst_sel:BYTE_3 dst_unused:UNUSED_PAD src0_sel:DWORD
	v_rndne_f32_e32 v65, v65
	v_cvt_i32_f32_e32 v68, v68
	v_cvt_i32_f32_sdwa v76, v76 dst_sel:WORD_1 dst_unused:UNUSED_PAD src0_sel:DWORD
	v_rndne_f32_e32 v69, v69
	v_rndne_f32_e32 v77, v77
	v_cvt_i32_f32_e32 v84, v84
; __device__ __forceinline__ void cvt_item_i8(const float* src, int ld, int k0, int c0, unsigned char* dst, int Kd, int drow0, const float* cmx  , unsigned char* scr, int lane) {
;     ...
;     for (int g = 0; g < 4; ++g)
; #pragma unroll
;         for (int i = 0; i < 4; ++i) *(unsigned*)(scr + (4 * c + i) * 132 + 32 * g + 4 * q) = pack_i8x4(v[g][0][i] * inv[i], v[g][1][i] * inv[i], v[g][2][i] * inv[i], v[g][3][i] * inv[i]);
;     asm volatile("s_waitcnt lgkmcnt(0)" ::: "memory");
; #pragma unroll
;     for (int r = 0; r < 4; ++r) { const int n = 8 * r + (lane >> 3), ch = lane & 7; const unsigned char* p = scr + n * 132 + ch * 16;
;         u32x4 o; o.x = *(const unsigned*)(p); o.y = *(const unsigned*)(p + 4); o.z = *(const unsigned*)(p + 8); o.w = *(const unsigned*)(p + 12);
;         *(u32x4*)(dst + (size_t)(drow0 + n) * Kd + k0 + 16 * ch) = o; }
;     asm volatile("s_waitcnt lgkmcnt(0)" ::: "memory");
	v_cvt_i32_f32_sdwa v91, v91 dst_sel:WORD_1 dst_unused:UNUSED_PAD src0_sel:DWORD
	v_rndne_f32_e32 v85, v85
	v_rndne_f32_e32 v92, v92
	v_cvt_i32_f32_e32 v37, v37
	v_cvt_i32_f32_sdwa v45, v45 dst_sel:WORD_1 dst_unused:UNUSED_PAD src0_sel:DWORD
	v_cvt_i32_f32_e32 v53, v53
	v_cvt_i32_f32_sdwa v61, v61 dst_sel:WORD_1 dst_unused:UNUSED_PAD src0_sel:DWORD
	v_cvt_i32_f32_e32 v73, v73
	v_cvt_i32_f32_e32 v89, v89
	v_lshlrev_b32_e32 v34, 8, v34
	v_lshlrev_b32_e32 v50, 8, v50
	v_cvt_i32_f32_sdwa v79, v79 dst_sel:BYTE_3 dst_unused:UNUSED_PAD src0_sel:DWORD
	v_rndne_f32_e32 v81, v81
	v_cvt_i32_f32_sdwa v31, v31 dst_sel:BYTE_3 dst_unused:UNUSED_PAD src0_sel:DWORD
	v_rndne_f32_e32 v32, v32
	v_cvt_i32_f32_sdwa v49, v49 dst_sel:BYTE_3 dst_unused:UNUSED_PAD src0_sel:DWORD
	v_cvt_i32_f32_sdwa v65, v65 dst_sel:BYTE_3 dst_unused:UNUSED_PAD src0_sel:DWORD
	v_cvt_i32_f32_e32 v69, v69
	v_cvt_i32_f32_sdwa v77, v77 dst_sel:WORD_1 dst_unused:UNUSED_PAD src0_sel:DWORD
	v_cvt_i32_f32_e32 v85, v85
	v_cvt_i32_f32_sdwa v92, v92 dst_sel:WORD_1 dst_unused:UNUSED_PAD src0_sel:DWORD
	v_and_b32_e32 v38, 0xff0000, v38
	v_and_b32_e32 v54, 0xff0000, v54
	v_lshlrev_b32_e32 v66, 8, v66
	v_lshlrev_b32_e32 v82, 8, v82
	v_perm_b32 v33, v34, v33, s37
	v_lshlrev_b32_e32 v34, 8, v39
	v_and_b32_e32 v39, 0xff0000, v43
	v_perm_b32 v43, v50, v48, s37
	v_lshlrev_b32_e32 v48, 8, v55
	v_cvt_i32_f32_sdwa v81, v81 dst_sel:BYTE_3 dst_unused:UNUSED_PAD src0_sel:DWORD
	v_cvt_i32_f32_sdwa v32, v32 dst_sel:BYTE_3 dst_unused:UNUSED_PAD src0_sel:DWORD
	v_and_b32_e32 v70, 0xff0000, v70
	v_and_b32_e32 v86, 0xff0000, v86
	v_and_b32_e32 v50, 0xff0000, v59
	v_perm_b32 v55, v66, v64, s37
	v_lshlrev_b32_e32 v59, 8, v71
	v_perm_b32 v66, v82, v80, s37
	v_lshlrev_b32_e32 v71, 8, v87
	v_or3_b32 v33, v33, v38, v42
	v_perm_b32 v34, v34, v35, s37
	v_lshlrev_b32_e32 v35, 8, v40
	v_or3_b32 v40, v43, v54, v58
	v_perm_b32 v42, v48, v51, s37
	v_lshlrev_b32_e32 v43, 8, v56
	v_and_b32_e32 v64, 0xff0000, v75
	v_and_b32_e32 v75, 0xff0000, v90
	v_and_b32_e32 v38, 0xff0000, v44
	v_and_b32_e32 v44, 0xff0000, v60
	v_or3_b32 v48, v55, v70, v74
	v_perm_b32 v51, v59, v67, s37
	v_lshlrev_b32_e32 v54, 8, v72
	v_or3_b32 v29, v66, v86, v29
	v_perm_b32 v56, v71, v83, s37
	v_lshlrev_b32_e32 v58, 8, v88
	v_or3_b32 v34, v34, v39, v46
	v_perm_b32 v35, v35, v36, s37
	v_lshlrev_b32_e32 v36, 8, v41
	ds_write2_b32 v21, v33, v40 offset1:8
	v_or3_b32 v33, v42, v50, v62
	v_perm_b32 v40, v43, v52, s37
	v_lshlrev_b32_e32 v41, 8, v57
	v_and_b32_e32 v55, 0xff0000, v76
	v_and_b32_e32 v59, 0xff0000, v91
	v_and_b32_e32 v39, 0xff0000, v45
	v_and_b32_e32 v42, 0xff0000, v61
	v_or3_b32 v43, v51, v64, v78
	v_perm_b32 v45, v54, v68, s37
	v_lshlrev_b32_e32 v46, 8, v73
	ds_write2_b32 v21, v48, v29 offset0:16 offset1:24
	v_or3_b32 v29, v56, v75, v30
	v_perm_b32 v30, v58, v84, s37
	v_lshlrev_b32_e32 v48, 8, v89
	v_or3_b32 v35, v35, v38, v47
	v_perm_b32 v36, v36, v37, s37
	ds_write2_b32 v21, v34, v33 offset0:33 offset1:41
	v_or3_b32 v33, v40, v44, v63
	v_perm_b32 v34, v41, v53, s37
	v_and_b32_e32 v50, 0xff0000, v77
	v_and_b32_e32 v51, 0xff0000, v92
	v_or3_b32 v37, v45, v55, v79
	v_perm_b32 v38, v46, v69, s37
	ds_write2_b32 v21, v43, v29 offset0:49 offset1:57
	v_or3_b32 v29, v30, v59, v31
	v_perm_b32 v30, v48, v85, s37
	v_or3_b32 v31, v36, v39, v49
	ds_write2_b32 v21, v35, v33 offset0:66 offset1:74
	v_or3_b32 v33, v34, v42, v65
	v_or3_b32 v34, v38, v50, v81
	ds_write2_b32 v21, v37, v29 offset0:82 offset1:90
	v_or3_b32 v29, v30, v51, v32
	ds_write2_b32 v21, v31, v33 offset0:99 offset1:107
	ds_write2_b32 v21, v34, v29 offset0:115 offset1:123
	s_waitcnt lgkmcnt(0)
	ds_read2_b32 v[30:31], v22 offset1:1
	ds_read2_b32 v[32:33], v22 offset0:2 offset1:3
	ds_read2_b32 v[34:35], v23 offset1:1
	ds_read2_b32 v[36:37], v24 offset1:1
	ds_read2_b32 v[38:39], v25 offset1:1
	ds_read2_b32 v[40:41], v26 offset1:1
	ds_read2_b32 v[42:43], v27 offset1:1
	ds_read2_b32 v[44:45], v28 offset1:1
	s_waitcnt lgkmcnt(6)
	global_store_dwordx4 v[10:11], v[30:33], off
	s_waitcnt lgkmcnt(4)
	global_store_dwordx4 v[12:13], v[34:37], off
	s_waitcnt lgkmcnt(2)
	global_store_dwordx4 v[14:15], v[38:41], off
	s_waitcnt lgkmcnt(0)
	global_store_dwordx4 v[6:7], v[42:45], off
	s_waitcnt lgkmcnt(0)
	s_cbranch_scc1 .LBB0_1909

; template <int GRP>
; __device__ __forceinline__ void conv_item(Frame& F, int r) {
;     ...
;     else { constexpr int KBN = (GRP == 3) ? 16 : CMS_KB, I_E = KBN * 88; const int up = r / (8 * I_E); r %= (8 * I_E); const int e = r / I_E; r %= I_E; const int kb = r / 88, nb = r % 88, n0 = nb * 32, drow = (n0 >> 7) * 256 + up * 128 + (n0 & 127);
;         if (GRP == 3) cvt_item_i8(inptr(F, up ? IN_MU : IN_MG) + (size_t)e * D * DFE, DFE, kb * 128, n0, ws + WS_MGU + (size_t)e * 2 * DFE * D, D, drow, cmx + 2 * DFF + e * 2 * DFE + drow, scr, F.lane);
; template <int L>
; __device__ __forceinline__ void layer(Frame& F, const XcdBarrier& bar, float* out, const int lo, const int hi) {
;     ...
;         if (cls == 3) { conv_all<GRP>(F, (F.G == 256) ? ((L == 0) ? SLOT_FIRST0 : SLOT_FIRST1) : 0); if (L == 0 && F.G == 256) { const int e4 = F.gw - G4_SLACK0; if (e4 >= 0 && e4 < G4_TAIL) conv_item<4>(F, 2048 + e4); } __syncthreads(); }
.LBB0_2031:
	v_readlane_b32 s0, v255, 27
	s_cmp_eq_u32 s0, 3
	s_barrier
	s_cbranch_scc0 .LBB0_2036
	s_cmpk_eq_i32 s48, 0x100
	s_cselect_b32 s0, 0x1800, 0
	v_readlane_b32 s1, v255, 10
	s_add_i32 s3, s0, s1
	s_cmpk_gt_i32 s3, 0x57ff
	v_readlane_b32 s40, v255, 13
	s_cbranch_scc1 .LBB0_2035
	v_readlane_b32 s0, v255, 9
	s_mulk_i32 s0, 0x2200
	s_add_i32 s0, s0, 0
	v_and_b32_e32 v2, 7, v0
	s_add_u32 s4, s50, 0x8200000
	s_waitcnt vmcnt(5)
	v_lshrrev_b32_e32 v1, 3, v194
	v_lshlrev_b32_e32 v4, 2, v2
	v_mul_u32_u24_e32 v7, 0x210, v2
	v_lshlrev_b32_e32 v2, 4, v2
	s_addc_u32 s12, s51, 0
	v_lshlrev_b32_e32 v16, 2, v1
	v_add_u32_e32 v8, s0, v2
	v_mul_u32_u24_e32 v9, 0x84, v1
	s_add_u32 s13, s50, 0x8b000
	v_mov_b32_e32 v3, 0
	v_add_u32_e32 v6, s0, v16
	v_add_u32_e32 v22, v8, v9
	s_addc_u32 s14, s51, 0
	v_or_b32_e32 v17, 8, v1
	v_or_b32_e32 v18, 16, v1
	v_or_b32_e32 v19, 24, v1
	s_movk_i32 s15, 0xa0
	v_lshlrev_b32_e32 v4, 2, v4
	v_mov_b32_e32 v5, v3
	s_mov_b32 s16, 0x42fe0000
	s_movk_i32 s17, 0x2000
	s_movk_i32 s18, 0x5000
	s_mov_b32 s19, 0x8000
	s_mov_b32 s20, 0x58000
	s_mov_b32 s21, 0x5a000
	s_mov_b32 s22, 0x5d000
	s_mov_b32 s23, 0x60000
	s_mov_b32 s24, 0xb0000
	s_mov_b32 s25, 0xb2000
	s_mov_b32 s26, 0xb5000
	s_mov_b32 s27, 0xb8000
	s_mov_b32 s28, 0x108000
	s_mov_b32 s29, 0x10a000
	s_mov_b32 s30, 0x10d000
	s_mov_b32 s31, 0x110000
	s_mov_b32 s34, 0xc2fe0000
	v_mov_b32_e32 v20, 0x42fe0000
	s_mov_b32 s35, 0xc0c0500
	v_add_u32_e32 v21, v6, v7
	v_add_u32_e32 v23, 0x420, v22
	v_add_u32_e32 v24, 0x428, v22
	v_add_u32_e32 v25, 0x840, v22
	v_add_u32_e32 v26, 0x848, v22
	v_add_u32_e32 v27, 0xc60, v22
	v_add_u32_e32 v28, 0xc68, v22
	v_readlane_b32 s0, v255, 9
	s_cmp_lt_u32 s0, 4
	s_cbranch_scc1 .Lstg_2034
	s_sleep 44
